# v99 + lever 9: the 32 never-taken s_cbranch_execz of the attention tile loops removed (exec is never zero there; falling through is equivalent)
# speedup vs baseline: 1.0106x; 1.0039x over previous
.LBB0_499:
	s_waitcnt lgkmcnt(7)
	v_mfma_f32_32x32x16_bf16 v[82:97], v[80:83], v[162:165], 0
	s_waitcnt lgkmcnt(6)
	v_mfma_f32_32x32x16_bf16 v[98:113], v[98:101], v[162:165], 0
	s_waitcnt lgkmcnt(5)
	v_mfma_f32_32x32x16_bf16 v[82:97], v[132:135], v[166:169], v[82:97]
	s_waitcnt lgkmcnt(4)
	v_mfma_f32_32x32x16_bf16 v[98:113], v[76:79], v[166:169], v[98:113]
	s_waitcnt lgkmcnt(3)
	v_mfma_f32_32x32x16_bf16 v[82:97], v[128:131], v[170:173], v[82:97]
	s_waitcnt lgkmcnt(2)
	v_mfma_f32_32x32x16_bf16 v[98:113], v[68:71], v[170:173], v[98:113]
	s_waitcnt lgkmcnt(1)
	v_mfma_f32_32x32x16_bf16 v[82:97], v[72:75], v[174:177], v[82:97]
	s_waitcnt lgkmcnt(0)
	v_mfma_f32_32x32x16_bf16 v[98:113], v[64:67], v[174:177], v[98:113]
	s_barrier
	v_cndmask_b32_e64 v64, 0, 1, s[40:41]
	v_cmp_ne_u32_e64 s[42:43], 1, v64
	s_andn2_b64 vcc, exec, s[40:41]
	s_mov_b64 s[2:3], -1
	s_cbranch_vccnz .LBB0_503
	s_nop 3
	v_exp_f32_e32 v64, v82
	v_exp_f32_e32 v65, v83
	v_exp_f32_e32 v66, v84
	v_exp_f32_e32 v67, v85
	v_exp_f32_e32 v68, v86
	v_exp_f32_e32 v69, v87
	v_exp_f32_e32 v70, v88
	v_exp_f32_e32 v71, v89
	v_exp_f32_e32 v72, v90
	v_exp_f32_e32 v73, v91
	v_exp_f32_e32 v74, v92
	v_exp_f32_e32 v75, v93
	v_exp_f32_e32 v76, v94
	v_exp_f32_e32 v77, v95
	v_exp_f32_e32 v78, v96
.LBB0_501:
	s_and_b64 vcc, exec, s[42:43]
	s_mov_b64 s[2:3], -1
	s_cbranch_vccnz .LBB0_505
.LBB0_502:
	s_nop 0
	v_exp_f32_e32 v80, v98
	v_exp_f32_e32 v81, v99
	v_exp_f32_e32 v82, v100
	v_exp_f32_e32 v83, v101
	v_exp_f32_e32 v84, v102
	v_exp_f32_e32 v85, v103
	v_exp_f32_e32 v86, v104
	v_exp_f32_e32 v87, v105
	v_exp_f32_e32 v88, v106
	v_exp_f32_e32 v89, v107
	v_exp_f32_e32 v90, v108
	v_exp_f32_e32 v91, v109
	v_exp_f32_e32 v92, v110
	v_exp_f32_e32 v93, v111
	v_exp_f32_e32 v94, v112
.LBB0_507:
	v_exp_f32_e32 v79, v97
	v_exp_f32_e32 v95, v113
	v_cvt_pk_bf16_f32 v96, v64, v65
	v_cvt_pk_bf16_f32 v97, v66, v67
	v_cvt_pk_bf16_f32 v98, v68, v69
	v_cvt_pk_bf16_f32 v99, v70, v71
	v_cvt_pk_bf16_f32 v100, v72, v73
	v_cvt_pk_bf16_f32 v101, v74, v75
	v_cvt_pk_bf16_f32 v102, v76, v77
	v_cvt_pk_bf16_f32 v103, v78, v79
	v_cvt_pk_bf16_f32 v104, v80, v81
	v_cvt_pk_bf16_f32 v105, v82, v83
	v_cvt_pk_bf16_f32 v106, v84, v85
	v_cvt_pk_bf16_f32 v107, v86, v87
	v_cvt_pk_bf16_f32 v108, v88, v89
	v_cvt_pk_bf16_f32 v109, v90, v91
	v_cvt_pk_bf16_f32 v110, v92, v93
	v_cvt_pk_bf16_f32 v111, v94, v95
	v_permlane32_swap_b32_e32 v96, v98
	v_permlane32_swap_b32_e32 v97, v99
	v_permlane32_swap_b32_e32 v100, v102
	v_permlane32_swap_b32_e32 v101, v103
	v_permlane32_swap_b32_e32 v104, v106
	v_permlane32_swap_b32_e32 v105, v107
	v_permlane32_swap_b32_e32 v108, v110
	v_permlane32_swap_b32_e32 v109, v111
	s_cmp_lt_u32 s63, 30
	s_waitcnt vmcnt(0)
	s_cselect_b64 s[22:23], -1, 0
	s_cmp_gt_u32 s63, 29
	s_cselect_b64 s[2:3], -1, 0
	s_and_b64 vcc, exec, s[2:3]
	s_waitcnt vmcnt(2)
	ds_write_b128 v211, v[178:181] offset:49152
	s_waitcnt vmcnt(1)
	ds_write_b128 v213, v[182:185] offset:16384
	s_waitcnt vmcnt(0)
	ds_write_b128 v214, v[186:189] offset:16384
	s_waitcnt lgkmcnt(0)
	s_barrier
	s_cbranch_vccnz .LBB0_509
	v_add_co_u32_e32 v112, vcc, 0x64d0000, v140
	s_nop 1
	v_addc_co_u32_e32 v113, vcc, 0, v141, vcc
	v_add_co_u32_e32 v114, vcc, 0x64d0000, v138
	s_nop 1
	v_addc_co_u32_e32 v115, vcc, 0, v139, vcc
	global_load_dwordx4 v[178:181], v[112:113], off offset:1024
	global_load_dwordx4 v[182:185], v[114:115], off offset:2048
	v_add_co_u32_e32 v112, vcc, 0x64d0000, v136
	s_nop 1
	v_addc_co_u32_e32 v113, vcc, 0, v137, vcc
	global_load_dwordx4 v[186:189], v[112:113], off offset:2048
.LBB0_509:
	ds_read_b128 v[112:115], v142 offset:49152
	ds_read_b128 v[128:131], v142 offset:57344
	ds_read_b128 v[146:149], v143 offset:49152
	ds_read_b128 v[150:153], v143 offset:57344
	ds_read_b128 v[154:157], v144 offset:49152
	ds_read_b128 v[218:221], v144 offset:57344
	ds_read_b128 v[222:225], v145 offset:49152
	ds_read_b128 v[226:229], v145 offset:57344
	ds_read_b64_tr_b16 v[116:117], v212 offset:0
	ds_read_b64_tr_b16 v[118:119], v212 offset:0x800
	ds_read_b64_tr_b16 v[120:121], v212 offset:0x1000
	ds_read_b64_tr_b16 v[122:123], v212 offset:0x1800
	ds_read_b64_tr_b16 v[124:125], v212 offset:0x2000
	ds_read_b64_tr_b16 v[126:127], v212 offset:0x2800
	ds_read_b64_tr_b16 v[132:133], v212 offset:0x3000
	ds_read_b64_tr_b16 v[134:135], v212 offset:0x3800
	s_waitcnt lgkmcnt(0)
	s_nop 0
	v_mfma_f32_32x32x16_bf16 v[0:15], v[96:99], v[116:119], v[0:15]
	ds_read_b64_tr_b16 v[116:117], v212 offset:0x200
	ds_read_b64_tr_b16 v[118:119], v212 offset:0xa00
	v_mfma_f32_32x32x16_bf16 v[0:15], v[100:103], v[120:123], v[0:15]
	ds_read_b64_tr_b16 v[120:121], v212 offset:0x1200
	ds_read_b64_tr_b16 v[122:123], v212 offset:0x1a00
	v_mfma_f32_32x32x16_bf16 v[0:15], v[104:107], v[124:127], v[0:15]
	ds_read_b64_tr_b16 v[124:125], v212 offset:0x2200
	ds_read_b64_tr_b16 v[126:127], v212 offset:0x2a00
	v_mfma_f32_32x32x16_bf16 v[0:15], v[108:111], v[132:135], v[0:15]
	ds_read_b64_tr_b16 v[132:133], v212 offset:0x3200
	ds_read_b64_tr_b16 v[134:135], v212 offset:0x3a00
	s_waitcnt lgkmcnt(0)
	v_mfma_f32_32x32x16_bf16 v[16:31], v[96:99], v[116:119], v[16:31]
	ds_read_b64_tr_b16 v[116:117], v212 offset:0x400
	ds_read_b64_tr_b16 v[118:119], v212 offset:0xc00
	v_mfma_f32_32x32x16_bf16 v[16:31], v[100:103], v[120:123], v[16:31]
	ds_read_b64_tr_b16 v[120:121], v212 offset:0x1400
	ds_read_b64_tr_b16 v[122:123], v212 offset:0x1c00
	v_mfma_f32_32x32x16_bf16 v[16:31], v[104:107], v[124:127], v[16:31]
	ds_read_b64_tr_b16 v[124:125], v212 offset:0x2400
	ds_read_b64_tr_b16 v[126:127], v212 offset:0x2c00
	v_mfma_f32_32x32x16_bf16 v[16:31], v[108:111], v[132:135], v[16:31]
	ds_read_b64_tr_b16 v[132:133], v212 offset:0x3400
	ds_read_b64_tr_b16 v[134:135], v212 offset:0x3c00
	s_waitcnt lgkmcnt(0)
	v_mfma_f32_32x32x16_bf16 v[32:47], v[96:99], v[116:119], v[32:47]
	ds_read_b64_tr_b16 v[116:117], v212 offset:0x600
	ds_read_b64_tr_b16 v[118:119], v212 offset:0xe00
	v_mfma_f32_32x32x16_bf16 v[32:47], v[100:103], v[120:123], v[32:47]
	ds_read_b64_tr_b16 v[120:121], v212 offset:0x1600
	ds_read_b64_tr_b16 v[122:123], v212 offset:0x1e00
	v_mfma_f32_32x32x16_bf16 v[32:47], v[104:107], v[124:127], v[32:47]
	ds_read_b64_tr_b16 v[124:125], v212 offset:0x2600
	ds_read_b64_tr_b16 v[126:127], v212 offset:0x2e00
	v_mfma_f32_32x32x16_bf16 v[32:47], v[108:111], v[132:135], v[32:47]
	ds_read_b64_tr_b16 v[132:133], v212 offset:0x3600
	ds_read_b64_tr_b16 v[134:135], v212 offset:0x3e00
	s_waitcnt lgkmcnt(0)
	v_mfma_f32_32x32x16_bf16 v[48:63], v[96:99], v[116:119], v[48:63]
	v_mfma_f32_32x32x16_bf16 v[48:63], v[100:103], v[120:123], v[48:63]
	v_mfma_f32_32x32x16_bf16 v[48:63], v[104:107], v[124:127], v[48:63]
	v_mfma_f32_32x32x16_bf16 v[48:63], v[108:111], v[132:135], v[48:63]
	s_waitcnt lgkmcnt(7)
	v_mfma_f32_32x32x16_bf16 v[112:127], v[112:115], v[162:165], 0
	s_waitcnt lgkmcnt(6)
	v_mfma_f32_32x32x16_bf16 v[128:143], v[128:131], v[162:165], 0
	s_waitcnt lgkmcnt(5)
	v_mfma_f32_32x32x16_bf16 v[112:127], v[146:149], v[166:169], v[112:127]
	s_waitcnt lgkmcnt(4)
	v_mfma_f32_32x32x16_bf16 v[128:143], v[150:153], v[166:169], v[128:143]
	s_waitcnt lgkmcnt(3)
	v_mfma_f32_32x32x16_bf16 v[112:127], v[154:157], v[170:173], v[112:127]
	s_waitcnt lgkmcnt(2)
	v_mfma_f32_32x32x16_bf16 v[128:143], v[218:221], v[170:173], v[128:143]
	s_waitcnt lgkmcnt(1)
	v_mfma_f32_32x32x16_bf16 v[112:127], v[222:225], v[174:177], v[112:127]
	s_waitcnt lgkmcnt(0)
	v_mfma_f32_32x32x16_bf16 v[128:143], v[226:229], v[174:177], v[128:143]
	s_barrier
	s_and_b64 vcc, exec, s[42:43]
	s_mov_b64 s[58:59], -1
	s_cbranch_vccnz .LBB0_513
	s_nop 5
	v_exp_f32_e32 v96, v112
	v_exp_f32_e32 v97, v113
	v_exp_f32_e32 v98, v114
	v_exp_f32_e32 v99, v115
	v_exp_f32_e32 v100, v116
	v_exp_f32_e32 v101, v117
	v_exp_f32_e32 v102, v118
	v_exp_f32_e32 v103, v119
	v_exp_f32_e32 v104, v120
	v_exp_f32_e32 v105, v121
	v_exp_f32_e32 v106, v122
	v_exp_f32_e32 v107, v123
	v_exp_f32_e32 v108, v124
	v_exp_f32_e32 v109, v125
	v_exp_f32_e32 v110, v126
.LBB0_511:
	s_and_b64 vcc, exec, s[42:43]
	s_mov_b64 s[42:43], -1
	s_cbranch_vccnz .LBB0_515
.LBB0_512:
	s_nop 2
	v_exp_f32_e32 v144, v128
	v_exp_f32_e32 v145, v129
	v_exp_f32_e32 v146, v130
	v_exp_f32_e32 v147, v131
	v_exp_f32_e32 v148, v132
	v_exp_f32_e32 v149, v133
	v_exp_f32_e32 v150, v134
	v_exp_f32_e32 v151, v135
	v_exp_f32_e32 v152, v136
	v_exp_f32_e32 v153, v137
	v_exp_f32_e32 v154, v138
	v_exp_f32_e32 v155, v139
	v_exp_f32_e32 v156, v140
	v_exp_f32_e32 v157, v141
	v_exp_f32_e32 v158, v142
.LBB0_517:
	v_exp_f32_e32 v111, v127
	v_exp_f32_e32 v159, v143
	v_cvt_pk_bf16_f32 v112, v96, v97
	v_cvt_pk_bf16_f32 v113, v98, v99
	v_cvt_pk_bf16_f32 v114, v100, v101
	v_cvt_pk_bf16_f32 v115, v102, v103
	v_cvt_pk_bf16_f32 v116, v104, v105
	v_cvt_pk_bf16_f32 v117, v106, v107
	v_cvt_pk_bf16_f32 v118, v108, v109
	v_cvt_pk_bf16_f32 v119, v110, v111
	v_cvt_pk_bf16_f32 v124, v144, v145
	v_cvt_pk_bf16_f32 v125, v146, v147
	v_cvt_pk_bf16_f32 v126, v148, v149
	v_cvt_pk_bf16_f32 v127, v150, v151
	v_cvt_pk_bf16_f32 v120, v152, v153
	v_cvt_pk_bf16_f32 v121, v154, v155
	v_cvt_pk_bf16_f32 v122, v156, v157
	v_cvt_pk_bf16_f32 v123, v158, v159
	v_permlane32_swap_b32_e32 v112, v114
	v_permlane32_swap_b32_e32 v113, v115
	v_permlane32_swap_b32_e32 v116, v118
	v_permlane32_swap_b32_e32 v117, v119
	v_permlane32_swap_b32_e32 v124, v126
	v_permlane32_swap_b32_e32 v125, v127
	v_permlane32_swap_b32_e32 v120, v122
	v_permlane32_swap_b32_e32 v121, v123
	s_andn2_b64 vcc, exec, s[22:23]
	s_cbranch_vccnz .LBB0_496
	s_waitcnt vmcnt(0)
	s_waitcnt vmcnt(2)
	ds_write_b128 v211, v[178:181] offset:32768
	s_waitcnt vmcnt(1)
	ds_write_b128 v213, v[182:185]
	s_waitcnt vmcnt(0)
	ds_write_b128 v214, v[186:189]
	s_branch .LBB0_496

.LBB0_523:
	v_lshl_add_u64 v[132:133], s[74:75], 0, v[192:193]
	v_add_co_u32_e32 v64, vcc, s67, v132
	v_lshl_add_u64 v[130:131], s[74:75], 0, v[194:195]
	s_nop 0
	v_addc_co_u32_e32 v65, vcc, 0, v133, vcc
	v_add_co_u32_e32 v66, vcc, s67, v130
	v_lshl_add_u64 v[128:129], s[74:75], 0, v[160:161]
	s_nop 0
	v_addc_co_u32_e32 v67, vcc, 0, v131, vcc
	global_load_dwordx4 v[146:149], v[64:65], off offset:1024
	global_load_dwordx4 v[150:153], v[66:67], off offset:2048
	v_add_co_u32_e32 v64, vcc, s67, v128
	s_nop 1
	v_addc_co_u32_e32 v65, vcc, 0, v129, vcc
	global_load_dwordx4 v[154:157], v[64:65], off offset:2048
	v_add_u32_e32 v134, v206, v207
	v_add_u32_e32 v135, v206, v208
	v_add_u32_e32 v136, v206, v209
	v_add_u32_e32 v137, v206, v210
	ds_read_b128 v[64:67], v134 offset:32768
	ds_read_b128 v[68:71], v134 offset:40960
	ds_read_b128 v[72:75], v135 offset:32768
	ds_read_b128 v[76:79], v135 offset:40960
	ds_read_b128 v[80:83], v136 offset:32768
	ds_read_b128 v[84:87], v136 offset:40960
	ds_read_b128 v[88:91], v137 offset:32768
	ds_read_b128 v[92:95], v137 offset:40960
	s_waitcnt lgkmcnt(7)
	v_mfma_f32_32x32x16_bf16 v[112:127], v[64:67], v[162:165], 0
	s_waitcnt lgkmcnt(6)
	v_mfma_f32_32x32x16_bf16 v[96:111], v[68:71], v[162:165], 0
	s_waitcnt lgkmcnt(5)
	v_mfma_f32_32x32x16_bf16 v[112:127], v[72:75], v[166:169], v[112:127]
	s_waitcnt lgkmcnt(4)
	v_mfma_f32_32x32x16_bf16 v[96:111], v[76:79], v[166:169], v[96:111]
	s_waitcnt lgkmcnt(3)
	v_mfma_f32_32x32x16_bf16 v[112:127], v[80:83], v[170:173], v[112:127]
	s_waitcnt lgkmcnt(2)
	v_mfma_f32_32x32x16_bf16 v[96:111], v[84:87], v[170:173], v[96:111]
	s_waitcnt lgkmcnt(1)
	v_mfma_f32_32x32x16_bf16 v[112:127], v[88:91], v[174:177], v[112:127]
	s_waitcnt lgkmcnt(0)
	v_mfma_f32_32x32x16_bf16 v[96:111], v[92:95], v[174:177], v[96:111]
	v_cndmask_b32_e64 v64, 0, 1, s[40:41]
	v_cmp_ne_u32_e64 s[42:43], 1, v64
	s_andn2_b64 vcc, exec, s[40:41]
	s_mov_b64 s[2:3], -1
	s_cbranch_vccnz .LBB0_527
	s_nop 4
	v_exp_f32_e32 v64, v112
	v_exp_f32_e32 v65, v113
	v_exp_f32_e32 v66, v114
	v_exp_f32_e32 v67, v115
	v_exp_f32_e32 v68, v116
	v_exp_f32_e32 v69, v117
	v_exp_f32_e32 v70, v118
	v_exp_f32_e32 v71, v119
	v_exp_f32_e32 v72, v120
	v_exp_f32_e32 v73, v121
	v_exp_f32_e32 v74, v122
	v_exp_f32_e32 v75, v123
	v_exp_f32_e32 v76, v124
	v_exp_f32_e32 v77, v125
	v_exp_f32_e32 v78, v126
.LBB0_525:
	s_and_b64 vcc, exec, s[42:43]
	s_mov_b64 s[2:3], -1
	s_cbranch_vccnz .LBB0_529
.LBB0_526:
	s_nop 1
	v_exp_f32_e32 v80, v96
	v_exp_f32_e32 v81, v97
	v_exp_f32_e32 v82, v98
	v_exp_f32_e32 v83, v99
	v_exp_f32_e32 v84, v100
	v_exp_f32_e32 v85, v101
	v_exp_f32_e32 v86, v102
	v_exp_f32_e32 v87, v103
	v_exp_f32_e32 v88, v104
	v_exp_f32_e32 v89, v105
	v_exp_f32_e32 v90, v106
	v_exp_f32_e32 v91, v107
	v_exp_f32_e32 v92, v108
	v_exp_f32_e32 v93, v109
	v_exp_f32_e32 v94, v110
.LBB0_531:
	v_exp_f32_e32 v79, v127
	v_exp_f32_e32 v95, v111
	v_cvt_pk_bf16_f32 v96, v64, v65
	v_cvt_pk_bf16_f32 v97, v66, v67
	v_cvt_pk_bf16_f32 v98, v68, v69
	v_cvt_pk_bf16_f32 v99, v70, v71
	v_cvt_pk_bf16_f32 v100, v72, v73
	v_cvt_pk_bf16_f32 v101, v74, v75
	v_cvt_pk_bf16_f32 v102, v76, v77
	v_cvt_pk_bf16_f32 v103, v78, v79
	v_cvt_pk_bf16_f32 v104, v80, v81
	v_cvt_pk_bf16_f32 v105, v82, v83
	v_cvt_pk_bf16_f32 v106, v84, v85
	v_cvt_pk_bf16_f32 v107, v86, v87
	v_cvt_pk_bf16_f32 v108, v88, v89
	v_cvt_pk_bf16_f32 v109, v90, v91
	v_cvt_pk_bf16_f32 v110, v92, v93
	v_cvt_pk_bf16_f32 v111, v94, v95
	v_permlane32_swap_b32_e32 v96, v98
	v_permlane32_swap_b32_e32 v97, v99
	v_permlane32_swap_b32_e32 v100, v102
	v_permlane32_swap_b32_e32 v101, v103
	v_permlane32_swap_b32_e32 v104, v106
	v_permlane32_swap_b32_e32 v105, v107
	v_permlane32_swap_b32_e32 v108, v110
	v_permlane32_swap_b32_e32 v109, v111
	s_barrier
	ds_read_b64_tr_b16 v[112:113], v212 offset:0
	ds_read_b64_tr_b16 v[114:115], v212 offset:0x800
	ds_read_b64_tr_b16 v[116:117], v212 offset:0x1000
	ds_read_b64_tr_b16 v[118:119], v212 offset:0x1800
	ds_read_b64_tr_b16 v[120:121], v212 offset:0x2000
	ds_read_b64_tr_b16 v[122:123], v212 offset:0x2800
	ds_read_b64_tr_b16 v[124:125], v212 offset:0x3000
	ds_read_b64_tr_b16 v[126:127], v212 offset:0x3800
	s_waitcnt lgkmcnt(0)
	s_nop 0
	v_mfma_f32_32x32x16_bf16 v[0:15], v[96:99], v[112:115], v[0:15]
	ds_read_b64_tr_b16 v[112:113], v212 offset:0x200
	ds_read_b64_tr_b16 v[114:115], v212 offset:0xa00
	v_mfma_f32_32x32x16_bf16 v[0:15], v[100:103], v[116:119], v[0:15]
	ds_read_b64_tr_b16 v[116:117], v212 offset:0x1200
	ds_read_b64_tr_b16 v[118:119], v212 offset:0x1a00
	v_mfma_f32_32x32x16_bf16 v[0:15], v[104:107], v[120:123], v[0:15]
	ds_read_b64_tr_b16 v[120:121], v212 offset:0x2200
	ds_read_b64_tr_b16 v[122:123], v212 offset:0x2a00
	v_mfma_f32_32x32x16_bf16 v[0:15], v[108:111], v[124:127], v[0:15]
	ds_read_b64_tr_b16 v[124:125], v212 offset:0x3200
	ds_read_b64_tr_b16 v[126:127], v212 offset:0x3a00
	s_waitcnt lgkmcnt(0)
	v_mfma_f32_32x32x16_bf16 v[16:31], v[96:99], v[112:115], v[16:31]
	ds_read_b64_tr_b16 v[112:113], v212 offset:0x400
	ds_read_b64_tr_b16 v[114:115], v212 offset:0xc00
	v_mfma_f32_32x32x16_bf16 v[16:31], v[100:103], v[116:119], v[16:31]
	ds_read_b64_tr_b16 v[116:117], v212 offset:0x1400
	ds_read_b64_tr_b16 v[118:119], v212 offset:0x1c00
	v_mfma_f32_32x32x16_bf16 v[16:31], v[104:107], v[120:123], v[16:31]
	ds_read_b64_tr_b16 v[120:121], v212 offset:0x2400
	ds_read_b64_tr_b16 v[122:123], v212 offset:0x2c00
	v_mfma_f32_32x32x16_bf16 v[16:31], v[108:111], v[124:127], v[16:31]
	ds_read_b64_tr_b16 v[124:125], v212 offset:0x3400
	ds_read_b64_tr_b16 v[126:127], v212 offset:0x3c00
	s_waitcnt lgkmcnt(0)
	v_mfma_f32_32x32x16_bf16 v[32:47], v[96:99], v[112:115], v[32:47]
	ds_read_b64_tr_b16 v[112:113], v212 offset:0x600
	ds_read_b64_tr_b16 v[114:115], v212 offset:0xe00
	v_mfma_f32_32x32x16_bf16 v[32:47], v[100:103], v[116:119], v[32:47]
	ds_read_b64_tr_b16 v[116:117], v212 offset:0x1600
	ds_read_b64_tr_b16 v[118:119], v212 offset:0x1e00
	v_mfma_f32_32x32x16_bf16 v[32:47], v[104:107], v[120:123], v[32:47]
	ds_read_b64_tr_b16 v[120:121], v212 offset:0x2600
	ds_read_b64_tr_b16 v[122:123], v212 offset:0x2e00
	v_mfma_f32_32x32x16_bf16 v[32:47], v[108:111], v[124:127], v[32:47]
	ds_read_b64_tr_b16 v[124:125], v212 offset:0x3600
	ds_read_b64_tr_b16 v[126:127], v212 offset:0x3e00
	s_waitcnt lgkmcnt(0)
	v_mfma_f32_32x32x16_bf16 v[48:63], v[96:99], v[112:115], v[48:63]
	s_cmp_lt_u32 s63, 30
	s_waitcnt vmcnt(0)
	s_cselect_b64 s[22:23], -1, 0
	s_cmp_gt_u32 s63, 29
	s_cselect_b64 s[2:3], -1, 0
	s_and_b64 vcc, exec, s[2:3]
	s_waitcnt vmcnt(2)
	ds_write_b128 v211, v[146:149] offset:49152
	s_waitcnt vmcnt(1)
	ds_write_b128 v213, v[150:153] offset:16384
	s_waitcnt vmcnt(0)
	ds_write_b128 v214, v[154:157] offset:16384
	v_mfma_f32_32x32x16_bf16 v[48:63], v[100:103], v[116:119], v[48:63]
	s_waitcnt lgkmcnt(0)
	s_barrier
	v_mfma_f32_32x32x16_bf16 v[48:63], v[104:107], v[120:123], v[48:63]
	v_mfma_f32_32x32x16_bf16 v[48:63], v[108:111], v[124:127], v[48:63]
	s_cbranch_vccnz .LBB0_533
	v_add_co_u32_e32 v96, vcc, 0x64d0000, v132
	s_nop 1
	v_addc_co_u32_e32 v97, vcc, 0, v133, vcc
	v_add_co_u32_e32 v98, vcc, 0x64d0000, v130
	s_nop 1
	v_addc_co_u32_e32 v99, vcc, 0, v131, vcc
	global_load_dwordx4 v[146:149], v[96:97], off offset:1024
	global_load_dwordx4 v[150:153], v[98:99], off offset:2048
	v_add_co_u32_e32 v96, vcc, 0x64d0000, v128
	s_nop 1
	v_addc_co_u32_e32 v97, vcc, 0, v129, vcc
	global_load_dwordx4 v[154:157], v[96:97], off offset:2048
.LBB0_533:
	ds_read_b128 v[96:99], v134 offset:49152
	ds_read_b128 v[100:103], v134 offset:57344
	ds_read_b128 v[104:107], v135 offset:49152
	ds_read_b128 v[108:111], v135 offset:57344
	ds_read_b128 v[178:181], v136 offset:49152
	ds_read_b128 v[182:185], v136 offset:57344
	ds_read_b128 v[186:189], v137 offset:49152
	ds_read_b128 v[196:199], v137 offset:57344
	s_waitcnt lgkmcnt(7)
	v_mfma_f32_32x32x16_bf16 v[114:129], v[96:99], v[162:165], 0
	s_waitcnt lgkmcnt(6)
	v_mfma_f32_32x32x16_bf16 v[130:145], v[100:103], v[162:165], 0
	s_waitcnt lgkmcnt(5)
	v_mfma_f32_32x32x16_bf16 v[114:129], v[104:107], v[166:169], v[114:129]
	s_waitcnt lgkmcnt(4)
	v_mfma_f32_32x32x16_bf16 v[130:145], v[108:111], v[166:169], v[130:145]
	s_waitcnt lgkmcnt(3)
	v_mfma_f32_32x32x16_bf16 v[114:129], v[178:181], v[170:173], v[114:129]
	s_waitcnt lgkmcnt(2)
	v_mfma_f32_32x32x16_bf16 v[130:145], v[182:185], v[170:173], v[130:145]
	s_waitcnt lgkmcnt(1)
	v_mfma_f32_32x32x16_bf16 v[114:129], v[186:189], v[174:177], v[114:129]
	s_waitcnt lgkmcnt(0)
	v_mfma_f32_32x32x16_bf16 v[130:145], v[196:199], v[174:177], v[130:145]
	s_and_b64 vcc, exec, s[42:43]
	s_mov_b64 s[58:59], -1
	s_cbranch_vccnz .LBB0_537
	s_nop 6
	v_exp_f32_e32 v96, v114
	v_exp_f32_e32 v97, v115
	v_exp_f32_e32 v98, v116
	v_exp_f32_e32 v99, v117
	v_exp_f32_e32 v100, v118
	v_exp_f32_e32 v101, v119
	v_exp_f32_e32 v102, v120
	v_exp_f32_e32 v103, v121
	v_exp_f32_e32 v104, v122
	v_exp_f32_e32 v105, v123
	v_exp_f32_e32 v106, v124
	v_exp_f32_e32 v107, v125
	v_exp_f32_e32 v108, v126
	v_exp_f32_e32 v109, v127
	v_exp_f32_e32 v110, v128
.LBB0_535:
	s_and_b64 vcc, exec, s[42:43]
	s_mov_b64 s[42:43], -1
	s_cbranch_vccnz .LBB0_539
.LBB0_536:
	s_nop 3
	v_exp_f32_e32 v112, v130
	v_exp_f32_e32 v113, v131
	v_exp_f32_e32 v114, v132
	v_exp_f32_e32 v115, v133
	v_exp_f32_e32 v116, v134
	v_exp_f32_e32 v117, v135
	v_exp_f32_e32 v118, v136
	v_exp_f32_e32 v119, v137
	v_exp_f32_e32 v120, v138
	v_exp_f32_e32 v121, v139
	v_exp_f32_e32 v122, v140
	v_exp_f32_e32 v123, v141
	v_exp_f32_e32 v124, v142
	v_exp_f32_e32 v125, v143
	v_exp_f32_e32 v126, v144
.LBB0_541:
	v_exp_f32_e32 v111, v129
	s_nop 0
	v_exp_f32_e32 v127, v145
	v_cvt_pk_bf16_f32 v128, v96, v97
	v_cvt_pk_bf16_f32 v129, v98, v99
	v_cvt_pk_bf16_f32 v130, v100, v101
	v_cvt_pk_bf16_f32 v131, v102, v103
	v_cvt_pk_bf16_f32 v132, v104, v105
	v_cvt_pk_bf16_f32 v133, v106, v107
	v_cvt_pk_bf16_f32 v134, v108, v109
	v_cvt_pk_bf16_f32 v135, v110, v111
	v_cvt_pk_bf16_f32 v136, v112, v113
	v_cvt_pk_bf16_f32 v137, v114, v115
	v_cvt_pk_bf16_f32 v138, v116, v117
	v_cvt_pk_bf16_f32 v139, v118, v119
	v_cvt_pk_bf16_f32 v140, v120, v121
	v_cvt_pk_bf16_f32 v141, v122, v123
	v_cvt_pk_bf16_f32 v142, v124, v125
	v_cvt_pk_bf16_f32 v143, v126, v127
	v_permlane32_swap_b32_e32 v128, v130
	v_permlane32_swap_b32_e32 v129, v131
	v_permlane32_swap_b32_e32 v132, v134
	v_permlane32_swap_b32_e32 v133, v135
	v_permlane32_swap_b32_e32 v136, v138
	v_permlane32_swap_b32_e32 v137, v139
	v_permlane32_swap_b32_e32 v140, v142
	v_permlane32_swap_b32_e32 v141, v143
	s_barrier
	ds_read_b64_tr_b16 v[178:179], v158 offset:0
	ds_read_b64_tr_b16 v[180:181], v158 offset:0x800
	ds_read_b64_tr_b16 v[182:183], v158 offset:0x1000
	ds_read_b64_tr_b16 v[184:185], v158 offset:0x1800
	ds_read_b64_tr_b16 v[186:187], v158 offset:0x2000
	ds_read_b64_tr_b16 v[188:189], v158 offset:0x2800
	ds_read_b64_tr_b16 v[196:197], v158 offset:0x3000
	ds_read_b64_tr_b16 v[198:199], v158 offset:0x3800
	s_waitcnt lgkmcnt(0)
	s_nop 0
	v_mfma_f32_32x32x16_bf16 v[0:15], v[128:131], v[178:181], v[0:15]
	ds_read_b64_tr_b16 v[178:179], v158 offset:0x200
	ds_read_b64_tr_b16 v[180:181], v158 offset:0xa00
	v_mfma_f32_32x32x16_bf16 v[0:15], v[132:135], v[182:185], v[0:15]
	ds_read_b64_tr_b16 v[182:183], v158 offset:0x1200
	ds_read_b64_tr_b16 v[184:185], v158 offset:0x1a00
	v_mfma_f32_32x32x16_bf16 v[0:15], v[136:139], v[186:189], v[0:15]
	ds_read_b64_tr_b16 v[186:187], v158 offset:0x2200
	ds_read_b64_tr_b16 v[188:189], v158 offset:0x2a00
	v_mfma_f32_32x32x16_bf16 v[0:15], v[140:143], v[196:199], v[0:15]
	ds_read_b64_tr_b16 v[196:197], v158 offset:0x3200
	ds_read_b64_tr_b16 v[198:199], v158 offset:0x3a00
	s_waitcnt lgkmcnt(0)
	v_mfma_f32_32x32x16_bf16 v[16:31], v[128:131], v[178:181], v[16:31]
	ds_read_b64_tr_b16 v[178:179], v158 offset:0x400
	ds_read_b64_tr_b16 v[180:181], v158 offset:0xc00
	v_mfma_f32_32x32x16_bf16 v[16:31], v[132:135], v[182:185], v[16:31]
	ds_read_b64_tr_b16 v[182:183], v158 offset:0x1400
	ds_read_b64_tr_b16 v[184:185], v158 offset:0x1c00
	v_mfma_f32_32x32x16_bf16 v[16:31], v[136:139], v[186:189], v[16:31]
	ds_read_b64_tr_b16 v[186:187], v158 offset:0x2400
	ds_read_b64_tr_b16 v[188:189], v158 offset:0x2c00
	v_mfma_f32_32x32x16_bf16 v[16:31], v[140:143], v[196:199], v[16:31]
	ds_read_b64_tr_b16 v[196:197], v158 offset:0x3400
	ds_read_b64_tr_b16 v[198:199], v158 offset:0x3c00
	s_waitcnt lgkmcnt(0)
	v_mfma_f32_32x32x16_bf16 v[32:47], v[128:131], v[178:181], v[32:47]
	ds_read_b64_tr_b16 v[178:179], v158 offset:0x600
	ds_read_b64_tr_b16 v[180:181], v158 offset:0xe00
	v_mfma_f32_32x32x16_bf16 v[32:47], v[132:135], v[182:185], v[32:47]
	ds_read_b64_tr_b16 v[182:183], v158 offset:0x1600
	ds_read_b64_tr_b16 v[184:185], v158 offset:0x1e00
	v_mfma_f32_32x32x16_bf16 v[32:47], v[136:139], v[186:189], v[32:47]
	ds_read_b64_tr_b16 v[186:187], v158 offset:0x2600
	ds_read_b64_tr_b16 v[188:189], v158 offset:0x2e00
	v_mfma_f32_32x32x16_bf16 v[32:47], v[140:143], v[196:199], v[32:47]
	ds_read_b64_tr_b16 v[196:197], v158 offset:0x3600
	ds_read_b64_tr_b16 v[198:199], v158 offset:0x3e00
	s_waitcnt lgkmcnt(0)
	v_mfma_f32_32x32x16_bf16 v[48:63], v[128:131], v[178:181], v[48:63]
	s_andn2_b64 vcc, exec, s[22:23]
	v_mfma_f32_32x32x16_bf16 v[48:63], v[132:135], v[182:185], v[48:63]
	v_mfma_f32_32x32x16_bf16 v[48:63], v[136:139], v[186:189], v[48:63]
	v_mfma_f32_32x32x16_bf16 v[48:63], v[140:143], v[196:199], v[48:63]
	s_cbranch_vccnz .LBB0_522
	s_waitcnt vmcnt(0)
	s_waitcnt vmcnt(2)
	ds_write_b128 v211, v[146:149] offset:32768
	s_waitcnt vmcnt(1)
	ds_write_b128 v213, v[150:153]
	s_waitcnt vmcnt(0)
	ds_write_b128 v214, v[154:157]
	s_branch .LBB0_522

.LBB0_550:
	s_waitcnt lgkmcnt(7)
	v_mfma_f32_32x32x16_bf16 v[82:97], v[80:83], v[162:165], 0
	s_waitcnt lgkmcnt(6)
	v_mfma_f32_32x32x16_bf16 v[98:113], v[98:101], v[162:165], 0
	s_waitcnt lgkmcnt(5)
	v_mfma_f32_32x32x16_bf16 v[82:97], v[132:135], v[166:169], v[82:97]
	s_waitcnt lgkmcnt(4)
	v_mfma_f32_32x32x16_bf16 v[98:113], v[76:79], v[166:169], v[98:113]
	s_waitcnt lgkmcnt(3)
	v_mfma_f32_32x32x16_bf16 v[82:97], v[128:131], v[170:173], v[82:97]
	s_waitcnt lgkmcnt(2)
	v_mfma_f32_32x32x16_bf16 v[98:113], v[68:71], v[170:173], v[98:113]
	s_waitcnt lgkmcnt(1)
	v_mfma_f32_32x32x16_bf16 v[82:97], v[72:75], v[174:177], v[82:97]
	s_waitcnt lgkmcnt(0)
	v_mfma_f32_32x32x16_bf16 v[98:113], v[64:67], v[174:177], v[98:113]
	s_barrier
	v_cndmask_b32_e64 v64, 0, 1, s[40:41]
	v_cmp_ne_u32_e64 s[42:43], 1, v64
	s_andn2_b64 vcc, exec, s[40:41]
	s_mov_b64 s[2:3], -1
	s_cbranch_vccnz .LBB0_554
	s_nop 3
	v_exp_f32_e32 v64, v82
	v_exp_f32_e32 v65, v83
	v_exp_f32_e32 v66, v84
	v_exp_f32_e32 v67, v85
	v_exp_f32_e32 v68, v86
	v_exp_f32_e32 v69, v87
	v_exp_f32_e32 v70, v88
	v_exp_f32_e32 v71, v89
	v_exp_f32_e32 v72, v90
	v_exp_f32_e32 v73, v91
	v_exp_f32_e32 v74, v92
	v_exp_f32_e32 v75, v93
	v_exp_f32_e32 v76, v94
	v_exp_f32_e32 v77, v95
	v_exp_f32_e32 v78, v96
.LBB0_552:
	s_and_b64 vcc, exec, s[42:43]
	s_mov_b64 s[2:3], -1
	s_cbranch_vccnz .LBB0_556
.LBB0_553:
	s_nop 0
	v_exp_f32_e32 v80, v98
	v_exp_f32_e32 v81, v99
	v_exp_f32_e32 v82, v100
	v_exp_f32_e32 v83, v101
	v_exp_f32_e32 v84, v102
	v_exp_f32_e32 v85, v103
	v_exp_f32_e32 v86, v104
	v_exp_f32_e32 v87, v105
	v_exp_f32_e32 v88, v106
	v_exp_f32_e32 v89, v107
	v_exp_f32_e32 v90, v108
	v_exp_f32_e32 v91, v109
	v_exp_f32_e32 v92, v110
	v_exp_f32_e32 v93, v111
	v_exp_f32_e32 v94, v112
.LBB0_558:
	v_exp_f32_e32 v79, v97
	v_exp_f32_e32 v95, v113
	v_cvt_pk_bf16_f32 v96, v64, v65
	v_cvt_pk_bf16_f32 v97, v66, v67
	v_cvt_pk_bf16_f32 v98, v68, v69
	v_cvt_pk_bf16_f32 v99, v70, v71
	v_cvt_pk_bf16_f32 v100, v72, v73
	v_cvt_pk_bf16_f32 v101, v74, v75
	v_cvt_pk_bf16_f32 v102, v76, v77
	v_cvt_pk_bf16_f32 v103, v78, v79
	v_cvt_pk_bf16_f32 v104, v80, v81
	v_cvt_pk_bf16_f32 v105, v82, v83
	v_cvt_pk_bf16_f32 v106, v84, v85
	v_cvt_pk_bf16_f32 v107, v86, v87
	v_cvt_pk_bf16_f32 v108, v88, v89
	v_cvt_pk_bf16_f32 v109, v90, v91
	v_cvt_pk_bf16_f32 v110, v92, v93
	v_cvt_pk_bf16_f32 v111, v94, v95
	v_permlane32_swap_b32_e32 v96, v98
	v_permlane32_swap_b32_e32 v97, v99
	v_permlane32_swap_b32_e32 v100, v102
	v_permlane32_swap_b32_e32 v101, v103
	v_permlane32_swap_b32_e32 v104, v106
	v_permlane32_swap_b32_e32 v105, v107
	v_permlane32_swap_b32_e32 v108, v110
	v_permlane32_swap_b32_e32 v109, v111
	s_cmp_lt_u32 s10, 30
	s_waitcnt vmcnt(0)
	s_cselect_b64 s[22:23], -1, 0
	s_cmp_gt_u32 s10, 29
	s_cselect_b64 s[2:3], -1, 0
	s_and_b64 vcc, exec, s[2:3]
	s_waitcnt vmcnt(2)
	ds_write_b128 v211, v[178:181] offset:49152
	s_waitcnt vmcnt(1)
	ds_write_b128 v213, v[182:185] offset:16384
	s_waitcnt vmcnt(0)
	ds_write_b128 v214, v[186:189] offset:16384
	s_waitcnt lgkmcnt(0)
	s_barrier
	s_cbranch_vccnz .LBB0_560
	v_add_co_u32_e32 v112, vcc, 0x64d0000, v140
	s_nop 1
	v_addc_co_u32_e32 v113, vcc, 0, v141, vcc
	v_add_co_u32_e32 v114, vcc, 0x64d0000, v138
	s_nop 1
	v_addc_co_u32_e32 v115, vcc, 0, v139, vcc
	global_load_dwordx4 v[178:181], v[112:113], off offset:1152
	global_load_dwordx4 v[182:185], v[114:115], off offset:2048
	v_add_co_u32_e32 v112, vcc, 0x64d0000, v136
	s_nop 1
	v_addc_co_u32_e32 v113, vcc, 0, v137, vcc
	global_load_dwordx4 v[186:189], v[112:113], off offset:2048
.LBB0_560:
	ds_read_b128 v[112:115], v142 offset:49152
	ds_read_b128 v[128:131], v142 offset:57344
	ds_read_b128 v[146:149], v143 offset:49152
	ds_read_b128 v[150:153], v143 offset:57344
	ds_read_b128 v[154:157], v144 offset:49152
	ds_read_b128 v[218:221], v144 offset:57344
	ds_read_b128 v[222:225], v145 offset:49152
	ds_read_b128 v[226:229], v145 offset:57344
	ds_read_b64_tr_b16 v[116:117], v212 offset:0
	ds_read_b64_tr_b16 v[118:119], v212 offset:0x800
	ds_read_b64_tr_b16 v[120:121], v212 offset:0x1000
	ds_read_b64_tr_b16 v[122:123], v212 offset:0x1800
	ds_read_b64_tr_b16 v[124:125], v212 offset:0x2000
	ds_read_b64_tr_b16 v[126:127], v212 offset:0x2800
	ds_read_b64_tr_b16 v[132:133], v212 offset:0x3000
	ds_read_b64_tr_b16 v[134:135], v212 offset:0x3800
	s_waitcnt lgkmcnt(0)
	s_nop 0
	v_mfma_f32_32x32x16_bf16 v[0:15], v[96:99], v[116:119], v[0:15]
	ds_read_b64_tr_b16 v[116:117], v212 offset:0x200
	ds_read_b64_tr_b16 v[118:119], v212 offset:0xa00
	v_mfma_f32_32x32x16_bf16 v[0:15], v[100:103], v[120:123], v[0:15]
	ds_read_b64_tr_b16 v[120:121], v212 offset:0x1200
	ds_read_b64_tr_b16 v[122:123], v212 offset:0x1a00
	v_mfma_f32_32x32x16_bf16 v[0:15], v[104:107], v[124:127], v[0:15]
	ds_read_b64_tr_b16 v[124:125], v212 offset:0x2200
	ds_read_b64_tr_b16 v[126:127], v212 offset:0x2a00
	v_mfma_f32_32x32x16_bf16 v[0:15], v[108:111], v[132:135], v[0:15]
	ds_read_b64_tr_b16 v[132:133], v212 offset:0x3200
	ds_read_b64_tr_b16 v[134:135], v212 offset:0x3a00
	s_waitcnt lgkmcnt(0)
	v_mfma_f32_32x32x16_bf16 v[16:31], v[96:99], v[116:119], v[16:31]
	ds_read_b64_tr_b16 v[116:117], v212 offset:0x400
	ds_read_b64_tr_b16 v[118:119], v212 offset:0xc00
	v_mfma_f32_32x32x16_bf16 v[16:31], v[100:103], v[120:123], v[16:31]
	ds_read_b64_tr_b16 v[120:121], v212 offset:0x1400
	ds_read_b64_tr_b16 v[122:123], v212 offset:0x1c00
	v_mfma_f32_32x32x16_bf16 v[16:31], v[104:107], v[124:127], v[16:31]
	ds_read_b64_tr_b16 v[124:125], v212 offset:0x2400
	ds_read_b64_tr_b16 v[126:127], v212 offset:0x2c00
	v_mfma_f32_32x32x16_bf16 v[16:31], v[108:111], v[132:135], v[16:31]
	ds_read_b64_tr_b16 v[132:133], v212 offset:0x3400
	ds_read_b64_tr_b16 v[134:135], v212 offset:0x3c00
	s_waitcnt lgkmcnt(0)
	v_mfma_f32_32x32x16_bf16 v[32:47], v[96:99], v[116:119], v[32:47]
	ds_read_b64_tr_b16 v[116:117], v212 offset:0x600
	ds_read_b64_tr_b16 v[118:119], v212 offset:0xe00
	v_mfma_f32_32x32x16_bf16 v[32:47], v[100:103], v[120:123], v[32:47]
	ds_read_b64_tr_b16 v[120:121], v212 offset:0x1600
	ds_read_b64_tr_b16 v[122:123], v212 offset:0x1e00
	v_mfma_f32_32x32x16_bf16 v[32:47], v[104:107], v[124:127], v[32:47]
	ds_read_b64_tr_b16 v[124:125], v212 offset:0x2600
	ds_read_b64_tr_b16 v[126:127], v212 offset:0x2e00
	v_mfma_f32_32x32x16_bf16 v[32:47], v[108:111], v[132:135], v[32:47]
	ds_read_b64_tr_b16 v[132:133], v212 offset:0x3600
	ds_read_b64_tr_b16 v[134:135], v212 offset:0x3e00
	s_waitcnt lgkmcnt(0)
	v_mfma_f32_32x32x16_bf16 v[48:63], v[96:99], v[116:119], v[48:63]
	v_mfma_f32_32x32x16_bf16 v[48:63], v[100:103], v[120:123], v[48:63]
	v_mfma_f32_32x32x16_bf16 v[48:63], v[104:107], v[124:127], v[48:63]
	v_mfma_f32_32x32x16_bf16 v[48:63], v[108:111], v[132:135], v[48:63]
	s_waitcnt lgkmcnt(7)
	v_mfma_f32_32x32x16_bf16 v[112:127], v[112:115], v[162:165], 0
	s_waitcnt lgkmcnt(6)
	v_mfma_f32_32x32x16_bf16 v[128:143], v[128:131], v[162:165], 0
	s_waitcnt lgkmcnt(5)
	v_mfma_f32_32x32x16_bf16 v[112:127], v[146:149], v[166:169], v[112:127]
	s_waitcnt lgkmcnt(4)
	v_mfma_f32_32x32x16_bf16 v[128:143], v[150:153], v[166:169], v[128:143]
	s_waitcnt lgkmcnt(3)
	v_mfma_f32_32x32x16_bf16 v[112:127], v[154:157], v[170:173], v[112:127]
	s_waitcnt lgkmcnt(2)
	v_mfma_f32_32x32x16_bf16 v[128:143], v[218:221], v[170:173], v[128:143]
	s_waitcnt lgkmcnt(1)
	v_mfma_f32_32x32x16_bf16 v[112:127], v[222:225], v[174:177], v[112:127]
	s_waitcnt lgkmcnt(0)
	v_mfma_f32_32x32x16_bf16 v[128:143], v[226:229], v[174:177], v[128:143]
	s_barrier
	s_and_b64 vcc, exec, s[42:43]
	s_mov_b64 s[58:59], -1
	s_cbranch_vccnz .LBB0_564
	s_nop 5
	v_exp_f32_e32 v96, v112
	v_exp_f32_e32 v97, v113
	v_exp_f32_e32 v98, v114
	v_exp_f32_e32 v99, v115
	v_exp_f32_e32 v100, v116
	v_exp_f32_e32 v101, v117
	v_exp_f32_e32 v102, v118
	v_exp_f32_e32 v103, v119
	v_exp_f32_e32 v104, v120
	v_exp_f32_e32 v105, v121
	v_exp_f32_e32 v106, v122
	v_exp_f32_e32 v107, v123
	v_exp_f32_e32 v108, v124
	v_exp_f32_e32 v109, v125
	v_exp_f32_e32 v110, v126
.LBB0_562:
	s_and_b64 vcc, exec, s[42:43]
	s_mov_b64 s[42:43], -1
	s_cbranch_vccnz .LBB0_566
.LBB0_563:
	s_nop 2
	v_exp_f32_e32 v144, v128
	v_exp_f32_e32 v145, v129
	v_exp_f32_e32 v146, v130
	v_exp_f32_e32 v147, v131
	v_exp_f32_e32 v148, v132
	v_exp_f32_e32 v149, v133
	v_exp_f32_e32 v150, v134
	v_exp_f32_e32 v151, v135
	v_exp_f32_e32 v152, v136
	v_exp_f32_e32 v153, v137
	v_exp_f32_e32 v154, v138
	v_exp_f32_e32 v155, v139
	v_exp_f32_e32 v156, v140
	v_exp_f32_e32 v157, v141
	v_exp_f32_e32 v158, v142
.LBB0_568:
	v_exp_f32_e32 v111, v127
	v_exp_f32_e32 v159, v143
	v_cvt_pk_bf16_f32 v112, v96, v97
	v_cvt_pk_bf16_f32 v113, v98, v99
	v_cvt_pk_bf16_f32 v114, v100, v101
	v_cvt_pk_bf16_f32 v115, v102, v103
	v_cvt_pk_bf16_f32 v116, v104, v105
	v_cvt_pk_bf16_f32 v117, v106, v107
	v_cvt_pk_bf16_f32 v118, v108, v109
	v_cvt_pk_bf16_f32 v119, v110, v111
	v_cvt_pk_bf16_f32 v124, v144, v145
	v_cvt_pk_bf16_f32 v125, v146, v147
	v_cvt_pk_bf16_f32 v126, v148, v149
	v_cvt_pk_bf16_f32 v127, v150, v151
	v_cvt_pk_bf16_f32 v120, v152, v153
	v_cvt_pk_bf16_f32 v121, v154, v155
	v_cvt_pk_bf16_f32 v122, v156, v157
	v_cvt_pk_bf16_f32 v123, v158, v159
	v_permlane32_swap_b32_e32 v112, v114
	v_permlane32_swap_b32_e32 v113, v115
	v_permlane32_swap_b32_e32 v116, v118
	v_permlane32_swap_b32_e32 v117, v119
	v_permlane32_swap_b32_e32 v124, v126
	v_permlane32_swap_b32_e32 v125, v127
	v_permlane32_swap_b32_e32 v120, v122
	v_permlane32_swap_b32_e32 v121, v123
	s_andn2_b64 vcc, exec, s[22:23]
	s_cbranch_vccnz .LBB0_547
	s_waitcnt vmcnt(0)
	s_waitcnt vmcnt(2)
	ds_write_b128 v211, v[178:181] offset:32768
	s_waitcnt vmcnt(1)
	ds_write_b128 v213, v[182:185]
	s_waitcnt vmcnt(0)
	ds_write_b128 v214, v[186:189]
	s_branch .LBB0_547

.LBB0_574:
	v_lshl_add_u64 v[132:133], s[90:91], 0, v[192:193]
	v_add_co_u32_e32 v64, vcc, s67, v132
	v_lshl_add_u64 v[130:131], s[90:91], 0, v[194:195]
	s_nop 0
	v_addc_co_u32_e32 v65, vcc, 0, v133, vcc
	v_add_co_u32_e32 v66, vcc, s67, v130
	v_lshl_add_u64 v[128:129], s[90:91], 0, v[160:161]
	s_nop 0
	v_addc_co_u32_e32 v67, vcc, 0, v131, vcc
	global_load_dwordx4 v[146:149], v[64:65], off offset:1152
	global_load_dwordx4 v[150:153], v[66:67], off offset:2048
	v_add_co_u32_e32 v64, vcc, s67, v128
	s_nop 1
	v_addc_co_u32_e32 v65, vcc, 0, v129, vcc
	global_load_dwordx4 v[154:157], v[64:65], off offset:2048
	v_add_u32_e32 v134, v206, v207
	v_add_u32_e32 v135, v206, v208
	v_add_u32_e32 v136, v206, v209
	v_add_u32_e32 v137, v206, v210
	ds_read_b128 v[64:67], v134 offset:32768
	ds_read_b128 v[68:71], v134 offset:40960
	ds_read_b128 v[72:75], v135 offset:32768
	ds_read_b128 v[76:79], v135 offset:40960
	ds_read_b128 v[80:83], v136 offset:32768
	ds_read_b128 v[84:87], v136 offset:40960
	ds_read_b128 v[88:91], v137 offset:32768
	ds_read_b128 v[92:95], v137 offset:40960
	s_waitcnt lgkmcnt(7)
	v_mfma_f32_32x32x16_bf16 v[112:127], v[64:67], v[162:165], 0
	s_waitcnt lgkmcnt(6)
	v_mfma_f32_32x32x16_bf16 v[96:111], v[68:71], v[162:165], 0
	s_waitcnt lgkmcnt(5)
	v_mfma_f32_32x32x16_bf16 v[112:127], v[72:75], v[166:169], v[112:127]
	s_waitcnt lgkmcnt(4)
	v_mfma_f32_32x32x16_bf16 v[96:111], v[76:79], v[166:169], v[96:111]
	s_waitcnt lgkmcnt(3)
	v_mfma_f32_32x32x16_bf16 v[112:127], v[80:83], v[170:173], v[112:127]
	s_waitcnt lgkmcnt(2)
	v_mfma_f32_32x32x16_bf16 v[96:111], v[84:87], v[170:173], v[96:111]
	s_waitcnt lgkmcnt(1)
	v_mfma_f32_32x32x16_bf16 v[112:127], v[88:91], v[174:177], v[112:127]
	s_waitcnt lgkmcnt(0)
	v_mfma_f32_32x32x16_bf16 v[96:111], v[92:95], v[174:177], v[96:111]
	v_cndmask_b32_e64 v64, 0, 1, s[40:41]
	v_cmp_ne_u32_e64 s[42:43], 1, v64
	s_andn2_b64 vcc, exec, s[40:41]
	s_mov_b64 s[2:3], -1
	s_cbranch_vccnz .LBB0_578
	s_nop 4
	v_exp_f32_e32 v64, v112
	v_exp_f32_e32 v65, v113
	v_exp_f32_e32 v66, v114
	v_exp_f32_e32 v67, v115
	v_exp_f32_e32 v68, v116
	v_exp_f32_e32 v69, v117
	v_exp_f32_e32 v70, v118
	v_exp_f32_e32 v71, v119
	v_exp_f32_e32 v72, v120
	v_exp_f32_e32 v73, v121
	v_exp_f32_e32 v74, v122
	v_exp_f32_e32 v75, v123
	v_exp_f32_e32 v76, v124
	v_exp_f32_e32 v77, v125
	v_exp_f32_e32 v78, v126
.LBB0_576:
	s_and_b64 vcc, exec, s[42:43]
	s_mov_b64 s[2:3], -1
	s_cbranch_vccnz .LBB0_580
.LBB0_577:
	s_nop 1
	v_exp_f32_e32 v80, v96
	v_exp_f32_e32 v81, v97
	v_exp_f32_e32 v82, v98
	v_exp_f32_e32 v83, v99
	v_exp_f32_e32 v84, v100
	v_exp_f32_e32 v85, v101
	v_exp_f32_e32 v86, v102
	v_exp_f32_e32 v87, v103
	v_exp_f32_e32 v88, v104
	v_exp_f32_e32 v89, v105
	v_exp_f32_e32 v90, v106
	v_exp_f32_e32 v91, v107
	v_exp_f32_e32 v92, v108
	v_exp_f32_e32 v93, v109
	v_exp_f32_e32 v94, v110
.LBB0_582:
	v_exp_f32_e32 v79, v127
	v_exp_f32_e32 v95, v111
	v_cvt_pk_bf16_f32 v96, v64, v65
	v_cvt_pk_bf16_f32 v97, v66, v67
	v_cvt_pk_bf16_f32 v98, v68, v69
	v_cvt_pk_bf16_f32 v99, v70, v71
	v_cvt_pk_bf16_f32 v100, v72, v73
	v_cvt_pk_bf16_f32 v101, v74, v75
	v_cvt_pk_bf16_f32 v102, v76, v77
	v_cvt_pk_bf16_f32 v103, v78, v79
	v_cvt_pk_bf16_f32 v104, v80, v81
	v_cvt_pk_bf16_f32 v105, v82, v83
	v_cvt_pk_bf16_f32 v106, v84, v85
	v_cvt_pk_bf16_f32 v107, v86, v87
	v_cvt_pk_bf16_f32 v108, v88, v89
	v_cvt_pk_bf16_f32 v109, v90, v91
	v_cvt_pk_bf16_f32 v110, v92, v93
	v_cvt_pk_bf16_f32 v111, v94, v95
	v_permlane32_swap_b32_e32 v96, v98
	v_permlane32_swap_b32_e32 v97, v99
	v_permlane32_swap_b32_e32 v100, v102
	v_permlane32_swap_b32_e32 v101, v103
	v_permlane32_swap_b32_e32 v104, v106
	v_permlane32_swap_b32_e32 v105, v107
	v_permlane32_swap_b32_e32 v108, v110
	v_permlane32_swap_b32_e32 v109, v111
	s_barrier
	ds_read_b64_tr_b16 v[112:113], v212 offset:0
	ds_read_b64_tr_b16 v[114:115], v212 offset:0x800
	ds_read_b64_tr_b16 v[116:117], v212 offset:0x1000
	ds_read_b64_tr_b16 v[118:119], v212 offset:0x1800
	ds_read_b64_tr_b16 v[120:121], v212 offset:0x2000
	ds_read_b64_tr_b16 v[122:123], v212 offset:0x2800
	ds_read_b64_tr_b16 v[124:125], v212 offset:0x3000
	ds_read_b64_tr_b16 v[126:127], v212 offset:0x3800
	s_waitcnt lgkmcnt(0)
	s_nop 0
	v_mfma_f32_32x32x16_bf16 v[0:15], v[96:99], v[112:115], v[0:15]
	ds_read_b64_tr_b16 v[112:113], v212 offset:0x200
	ds_read_b64_tr_b16 v[114:115], v212 offset:0xa00
	v_mfma_f32_32x32x16_bf16 v[0:15], v[100:103], v[116:119], v[0:15]
	ds_read_b64_tr_b16 v[116:117], v212 offset:0x1200
	ds_read_b64_tr_b16 v[118:119], v212 offset:0x1a00
	v_mfma_f32_32x32x16_bf16 v[0:15], v[104:107], v[120:123], v[0:15]
	ds_read_b64_tr_b16 v[120:121], v212 offset:0x2200
	ds_read_b64_tr_b16 v[122:123], v212 offset:0x2a00
	v_mfma_f32_32x32x16_bf16 v[0:15], v[108:111], v[124:127], v[0:15]
	ds_read_b64_tr_b16 v[124:125], v212 offset:0x3200
	ds_read_b64_tr_b16 v[126:127], v212 offset:0x3a00
	s_waitcnt lgkmcnt(0)
	v_mfma_f32_32x32x16_bf16 v[16:31], v[96:99], v[112:115], v[16:31]
	ds_read_b64_tr_b16 v[112:113], v212 offset:0x400
	ds_read_b64_tr_b16 v[114:115], v212 offset:0xc00
	v_mfma_f32_32x32x16_bf16 v[16:31], v[100:103], v[116:119], v[16:31]
	ds_read_b64_tr_b16 v[116:117], v212 offset:0x1400
	ds_read_b64_tr_b16 v[118:119], v212 offset:0x1c00
	v_mfma_f32_32x32x16_bf16 v[16:31], v[104:107], v[120:123], v[16:31]
	ds_read_b64_tr_b16 v[120:121], v212 offset:0x2400
	ds_read_b64_tr_b16 v[122:123], v212 offset:0x2c00
	v_mfma_f32_32x32x16_bf16 v[16:31], v[108:111], v[124:127], v[16:31]
	ds_read_b64_tr_b16 v[124:125], v212 offset:0x3400
	ds_read_b64_tr_b16 v[126:127], v212 offset:0x3c00
	s_waitcnt lgkmcnt(0)
	v_mfma_f32_32x32x16_bf16 v[32:47], v[96:99], v[112:115], v[32:47]
	ds_read_b64_tr_b16 v[112:113], v212 offset:0x600
	ds_read_b64_tr_b16 v[114:115], v212 offset:0xe00
	v_mfma_f32_32x32x16_bf16 v[32:47], v[100:103], v[116:119], v[32:47]
	ds_read_b64_tr_b16 v[116:117], v212 offset:0x1600
	ds_read_b64_tr_b16 v[118:119], v212 offset:0x1e00
	v_mfma_f32_32x32x16_bf16 v[32:47], v[104:107], v[120:123], v[32:47]
	ds_read_b64_tr_b16 v[120:121], v212 offset:0x2600
	ds_read_b64_tr_b16 v[122:123], v212 offset:0x2e00
	v_mfma_f32_32x32x16_bf16 v[32:47], v[108:111], v[124:127], v[32:47]
	ds_read_b64_tr_b16 v[124:125], v212 offset:0x3600
	ds_read_b64_tr_b16 v[126:127], v212 offset:0x3e00
	s_waitcnt lgkmcnt(0)
	v_mfma_f32_32x32x16_bf16 v[48:63], v[96:99], v[112:115], v[48:63]
	s_cmp_lt_u32 s6, 30
	s_waitcnt vmcnt(0)
	s_cselect_b64 s[22:23], -1, 0
	s_cmp_gt_u32 s6, 29
	s_cselect_b64 s[2:3], -1, 0
	s_and_b64 vcc, exec, s[2:3]
	s_waitcnt vmcnt(2)
	ds_write_b128 v211, v[146:149] offset:49152
	s_waitcnt vmcnt(1)
	ds_write_b128 v213, v[150:153] offset:16384
	s_waitcnt vmcnt(0)
	ds_write_b128 v214, v[154:157] offset:16384
	v_mfma_f32_32x32x16_bf16 v[48:63], v[100:103], v[116:119], v[48:63]
	s_waitcnt lgkmcnt(0)
	s_barrier
	v_mfma_f32_32x32x16_bf16 v[48:63], v[104:107], v[120:123], v[48:63]
	v_mfma_f32_32x32x16_bf16 v[48:63], v[108:111], v[124:127], v[48:63]
	s_cbranch_vccnz .LBB0_584
	v_add_co_u32_e32 v96, vcc, 0x64d0000, v132
	s_nop 1
	v_addc_co_u32_e32 v97, vcc, 0, v133, vcc
	v_add_co_u32_e32 v98, vcc, 0x64d0000, v130
	s_nop 1
	v_addc_co_u32_e32 v99, vcc, 0, v131, vcc
	global_load_dwordx4 v[146:149], v[96:97], off offset:1152
	global_load_dwordx4 v[150:153], v[98:99], off offset:2048
	v_add_co_u32_e32 v96, vcc, 0x64d0000, v128
	s_nop 1
	v_addc_co_u32_e32 v97, vcc, 0, v129, vcc
	global_load_dwordx4 v[154:157], v[96:97], off offset:2048
.LBB0_584:
	ds_read_b128 v[96:99], v134 offset:49152
	ds_read_b128 v[100:103], v134 offset:57344
	ds_read_b128 v[104:107], v135 offset:49152
	ds_read_b128 v[108:111], v135 offset:57344
	ds_read_b128 v[178:181], v136 offset:49152
	ds_read_b128 v[182:185], v136 offset:57344
	ds_read_b128 v[186:189], v137 offset:49152
	ds_read_b128 v[196:199], v137 offset:57344
	s_waitcnt lgkmcnt(7)
	v_mfma_f32_32x32x16_bf16 v[114:129], v[96:99], v[162:165], 0
	s_waitcnt lgkmcnt(6)
	v_mfma_f32_32x32x16_bf16 v[130:145], v[100:103], v[162:165], 0
	s_waitcnt lgkmcnt(5)
	v_mfma_f32_32x32x16_bf16 v[114:129], v[104:107], v[166:169], v[114:129]
	s_waitcnt lgkmcnt(4)
	v_mfma_f32_32x32x16_bf16 v[130:145], v[108:111], v[166:169], v[130:145]
	s_waitcnt lgkmcnt(3)
	v_mfma_f32_32x32x16_bf16 v[114:129], v[178:181], v[170:173], v[114:129]
	s_waitcnt lgkmcnt(2)
	v_mfma_f32_32x32x16_bf16 v[130:145], v[182:185], v[170:173], v[130:145]
	s_waitcnt lgkmcnt(1)
	v_mfma_f32_32x32x16_bf16 v[114:129], v[186:189], v[174:177], v[114:129]
	s_waitcnt lgkmcnt(0)
	v_mfma_f32_32x32x16_bf16 v[130:145], v[196:199], v[174:177], v[130:145]
	s_and_b64 vcc, exec, s[42:43]
	s_mov_b64 s[58:59], -1
	s_cbranch_vccnz .LBB0_588
	s_nop 6
	v_exp_f32_e32 v96, v114
	v_exp_f32_e32 v97, v115
	v_exp_f32_e32 v98, v116
	v_exp_f32_e32 v99, v117
	v_exp_f32_e32 v100, v118
	v_exp_f32_e32 v101, v119
	v_exp_f32_e32 v102, v120
	v_exp_f32_e32 v103, v121
	v_exp_f32_e32 v104, v122
	v_exp_f32_e32 v105, v123
	v_exp_f32_e32 v106, v124
	v_exp_f32_e32 v107, v125
	v_exp_f32_e32 v108, v126
	v_exp_f32_e32 v109, v127
	v_exp_f32_e32 v110, v128
.LBB0_586:
	s_and_b64 vcc, exec, s[42:43]
	s_mov_b64 s[42:43], -1
	s_cbranch_vccnz .LBB0_590
.LBB0_587:
	s_nop 3
	v_exp_f32_e32 v112, v130
	v_exp_f32_e32 v113, v131
	v_exp_f32_e32 v114, v132
	v_exp_f32_e32 v115, v133
	v_exp_f32_e32 v116, v134
	v_exp_f32_e32 v117, v135
	v_exp_f32_e32 v118, v136
	v_exp_f32_e32 v119, v137
	v_exp_f32_e32 v120, v138
	v_exp_f32_e32 v121, v139
	v_exp_f32_e32 v122, v140
	v_exp_f32_e32 v123, v141
	v_exp_f32_e32 v124, v142
	v_exp_f32_e32 v125, v143
	v_exp_f32_e32 v126, v144
.LBB0_592:
	v_exp_f32_e32 v111, v129
	s_nop 0
	v_exp_f32_e32 v127, v145
	v_cvt_pk_bf16_f32 v128, v96, v97
	v_cvt_pk_bf16_f32 v129, v98, v99
	v_cvt_pk_bf16_f32 v130, v100, v101
	v_cvt_pk_bf16_f32 v131, v102, v103
	v_cvt_pk_bf16_f32 v132, v104, v105
	v_cvt_pk_bf16_f32 v133, v106, v107
	v_cvt_pk_bf16_f32 v134, v108, v109
	v_cvt_pk_bf16_f32 v135, v110, v111
	v_cvt_pk_bf16_f32 v136, v112, v113
	v_cvt_pk_bf16_f32 v137, v114, v115
	v_cvt_pk_bf16_f32 v138, v116, v117
	v_cvt_pk_bf16_f32 v139, v118, v119
	v_cvt_pk_bf16_f32 v140, v120, v121
	v_cvt_pk_bf16_f32 v141, v122, v123
	v_cvt_pk_bf16_f32 v142, v124, v125
	v_cvt_pk_bf16_f32 v143, v126, v127
	v_permlane32_swap_b32_e32 v128, v130
	v_permlane32_swap_b32_e32 v129, v131
	v_permlane32_swap_b32_e32 v132, v134
	v_permlane32_swap_b32_e32 v133, v135
	v_permlane32_swap_b32_e32 v136, v138
	v_permlane32_swap_b32_e32 v137, v139
	v_permlane32_swap_b32_e32 v140, v142
	v_permlane32_swap_b32_e32 v141, v143
	s_barrier
	ds_read_b64_tr_b16 v[178:179], v158 offset:0
	ds_read_b64_tr_b16 v[180:181], v158 offset:0x800
	ds_read_b64_tr_b16 v[182:183], v158 offset:0x1000
	ds_read_b64_tr_b16 v[184:185], v158 offset:0x1800
	ds_read_b64_tr_b16 v[186:187], v158 offset:0x2000
	ds_read_b64_tr_b16 v[188:189], v158 offset:0x2800
	ds_read_b64_tr_b16 v[196:197], v158 offset:0x3000
	ds_read_b64_tr_b16 v[198:199], v158 offset:0x3800
	s_waitcnt lgkmcnt(0)
	s_nop 0
	v_mfma_f32_32x32x16_bf16 v[0:15], v[128:131], v[178:181], v[0:15]
	ds_read_b64_tr_b16 v[178:179], v158 offset:0x200
	ds_read_b64_tr_b16 v[180:181], v158 offset:0xa00
	v_mfma_f32_32x32x16_bf16 v[0:15], v[132:135], v[182:185], v[0:15]
	ds_read_b64_tr_b16 v[182:183], v158 offset:0x1200
	ds_read_b64_tr_b16 v[184:185], v158 offset:0x1a00
	v_mfma_f32_32x32x16_bf16 v[0:15], v[136:139], v[186:189], v[0:15]
	ds_read_b64_tr_b16 v[186:187], v158 offset:0x2200
	ds_read_b64_tr_b16 v[188:189], v158 offset:0x2a00
	v_mfma_f32_32x32x16_bf16 v[0:15], v[140:143], v[196:199], v[0:15]
	ds_read_b64_tr_b16 v[196:197], v158 offset:0x3200
	ds_read_b64_tr_b16 v[198:199], v158 offset:0x3a00
	s_waitcnt lgkmcnt(0)
	v_mfma_f32_32x32x16_bf16 v[16:31], v[128:131], v[178:181], v[16:31]
	ds_read_b64_tr_b16 v[178:179], v158 offset:0x400
	ds_read_b64_tr_b16 v[180:181], v158 offset:0xc00
	v_mfma_f32_32x32x16_bf16 v[16:31], v[132:135], v[182:185], v[16:31]
	ds_read_b64_tr_b16 v[182:183], v158 offset:0x1400
	ds_read_b64_tr_b16 v[184:185], v158 offset:0x1c00
	v_mfma_f32_32x32x16_bf16 v[16:31], v[136:139], v[186:189], v[16:31]
	ds_read_b64_tr_b16 v[186:187], v158 offset:0x2400
	ds_read_b64_tr_b16 v[188:189], v158 offset:0x2c00
	v_mfma_f32_32x32x16_bf16 v[16:31], v[140:143], v[196:199], v[16:31]
	ds_read_b64_tr_b16 v[196:197], v158 offset:0x3400
	ds_read_b64_tr_b16 v[198:199], v158 offset:0x3c00
	s_waitcnt lgkmcnt(0)
	v_mfma_f32_32x32x16_bf16 v[32:47], v[128:131], v[178:181], v[32:47]
	ds_read_b64_tr_b16 v[178:179], v158 offset:0x600
	ds_read_b64_tr_b16 v[180:181], v158 offset:0xe00
	v_mfma_f32_32x32x16_bf16 v[32:47], v[132:135], v[182:185], v[32:47]
	ds_read_b64_tr_b16 v[182:183], v158 offset:0x1600
	ds_read_b64_tr_b16 v[184:185], v158 offset:0x1e00
	v_mfma_f32_32x32x16_bf16 v[32:47], v[136:139], v[186:189], v[32:47]
	ds_read_b64_tr_b16 v[186:187], v158 offset:0x2600
	ds_read_b64_tr_b16 v[188:189], v158 offset:0x2e00
	v_mfma_f32_32x32x16_bf16 v[32:47], v[140:143], v[196:199], v[32:47]
	ds_read_b64_tr_b16 v[196:197], v158 offset:0x3600
	ds_read_b64_tr_b16 v[198:199], v158 offset:0x3e00
	s_waitcnt lgkmcnt(0)
	v_mfma_f32_32x32x16_bf16 v[48:63], v[128:131], v[178:181], v[48:63]
	s_andn2_b64 vcc, exec, s[22:23]
	v_mfma_f32_32x32x16_bf16 v[48:63], v[132:135], v[182:185], v[48:63]
	v_mfma_f32_32x32x16_bf16 v[48:63], v[136:139], v[186:189], v[48:63]
	v_mfma_f32_32x32x16_bf16 v[48:63], v[140:143], v[196:199], v[48:63]
	s_cbranch_vccnz .LBB0_573
	s_waitcnt vmcnt(0)
	s_waitcnt vmcnt(2)
	ds_write_b128 v211, v[146:149] offset:32768
	s_waitcnt vmcnt(1)
	ds_write_b128 v213, v[150:153]
	s_waitcnt vmcnt(0)
	ds_write_b128 v214, v[154:157]
	s_branch .LBB0_573

.LBB0_602:
	s_and_b32 s23, s22, 1
	s_cmp_eq_u32 s74, 0x2e8000
	s_movk_i32 s44, 0x4000
	s_cbranch_scc1 .LBB0_606
	s_lshl_b32 s44, s23, 14
	s_and_saveexec_b64 s[2:3], s[42:43]
	s_xor_b32 s45, s44, 0x4000
	s_add_i32 s45, s81, s45
	s_add_i32 m0, s45, 0x8000
	v_lshl_add_u64 v[64:65], v[232:233], 0, s[74:75]
	global_load_lds_dwordx4 v[64:65], off
	v_lshl_add_u64 v[64:65], v[234:235], 0, s[74:75]
	s_add_i32 m0, s45, 0xa000
	s_nop 0
	global_load_lds_dwordx4 v[64:65], off

.LBB0_606:
	v_lshl_add_u32 v64, v246, 8, 0
	v_add_u32_e32 v112, s44, v64
	v_add_u32_e32 v68, v112, v226
	v_add_u32_e32 v72, v112, v227
	ds_read_b128 v[64:67], v68 offset:32768
	ds_read_b128 v[68:71], v68 offset:40960
	ds_read_b128 v[96:99], v72 offset:32768
	ds_read_b128 v[100:103], v72 offset:40960
	s_waitcnt lgkmcnt(0)
	v_mfma_f32_32x32x16_bf16 v[114:129], v[64:67], v[162:165], 0
	v_mfma_f32_32x32x16_bf16 v[80:95], v[64:67], v[186:189], 0
	v_mfma_f32_32x32x16_bf16 v[130:145], v[68:71], v[162:165], 0
	v_mfma_f32_32x32x16_bf16 v[64:79], v[68:71], v[186:189], 0
	v_mfma_f32_32x32x16_bf16 v[114:129], v[96:99], v[166:169], v[114:129]
	v_mfma_f32_32x32x16_bf16 v[80:95], v[96:99], v[190:193], v[80:95]
	v_mfma_f32_32x32x16_bf16 v[130:145], v[100:103], v[166:169], v[130:145]
	v_mfma_f32_32x32x16_bf16 v[64:79], v[100:103], v[190:193], v[64:79]
	v_add_u32_e32 v100, v112, v238
	v_add_u32_e32 v108, v112, v239
	ds_read_b128 v[96:99], v100 offset:32768
	ds_read_b128 v[100:103], v100 offset:40960
	ds_read_b128 v[104:107], v108 offset:32768
	ds_read_b128 v[108:111], v108 offset:40960
	s_waitcnt lgkmcnt(0)
	v_mfma_f32_32x32x16_bf16 v[114:129], v[96:99], v[170:173], v[114:129]
	v_mfma_f32_32x32x16_bf16 v[80:95], v[96:99], v[194:197], v[80:95]
	v_mfma_f32_32x32x16_bf16 v[130:145], v[100:103], v[170:173], v[130:145]
	v_mfma_f32_32x32x16_bf16 v[64:79], v[100:103], v[194:197], v[64:79]
	v_mfma_f32_32x32x16_bf16 v[114:129], v[104:107], v[174:177], v[114:129]
	v_mfma_f32_32x32x16_bf16 v[80:95], v[104:107], v[198:201], v[80:95]
	v_mfma_f32_32x32x16_bf16 v[130:145], v[108:111], v[174:177], v[130:145]
	v_mfma_f32_32x32x16_bf16 v[64:79], v[108:111], v[198:201], v[64:79]
	v_add_u32_e32 v100, v112, v247
	v_add_u32_e32 v108, v112, v249
	ds_read_b128 v[96:99], v100 offset:32768
	ds_read_b128 v[100:103], v100 offset:40960
	ds_read_b128 v[104:107], v108 offset:32768
	ds_read_b128 v[108:111], v108 offset:40960
	s_waitcnt lgkmcnt(0)
	v_mfma_f32_32x32x16_bf16 v[114:129], v[96:99], v[178:181], v[114:129]
	v_mfma_f32_32x32x16_bf16 v[80:95], v[96:99], v[202:205], v[80:95]
	v_mfma_f32_32x32x16_bf16 v[130:145], v[100:103], v[178:181], v[130:145]
	v_mfma_f32_32x32x16_bf16 v[64:79], v[100:103], v[202:205], v[64:79]
	v_mfma_f32_32x32x16_bf16 v[114:129], v[104:107], v[182:185], v[114:129]
	v_mfma_f32_32x32x16_bf16 v[80:95], v[104:107], v[206:209], v[80:95]
	v_mfma_f32_32x32x16_bf16 v[130:145], v[108:111], v[182:185], v[130:145]
	v_mfma_f32_32x32x16_bf16 v[64:79], v[108:111], v[206:209], v[64:79]
	v_cndmask_b32_e64 v96, 0, 1, s[40:41]
	v_cmp_ne_u32_e64 s[44:45], 1, v96
	s_andn2_b64 vcc, exec, s[40:41]
	s_mov_b64 s[2:3], -1
	s_cbranch_vccnz .LBB0_610
	s_nop 3
	v_exp_f32_e32 v96, v114
	v_exp_f32_e32 v97, v115
	v_exp_f32_e32 v98, v116
	v_exp_f32_e32 v99, v117
	v_exp_f32_e32 v100, v118
	v_exp_f32_e32 v101, v119
	v_exp_f32_e32 v102, v120
	v_exp_f32_e32 v103, v121
	v_exp_f32_e32 v104, v122
	v_exp_f32_e32 v105, v123
	v_exp_f32_e32 v106, v124
	v_exp_f32_e32 v107, v125
	v_exp_f32_e32 v108, v126
	v_exp_f32_e32 v109, v127
	v_exp_f32_e32 v110, v128
.LBB0_608:
	s_and_b64 vcc, exec, s[44:45]
	s_mov_b64 s[2:3], -1
	s_cbranch_vccnz .LBB0_612
.LBB0_609:
	s_nop 0
	v_exp_f32_e32 v112, v130
	v_exp_f32_e32 v113, v131
	v_exp_f32_e32 v114, v132
	v_exp_f32_e32 v115, v133
	v_exp_f32_e32 v116, v134
	v_exp_f32_e32 v117, v135
	v_exp_f32_e32 v118, v136
	v_exp_f32_e32 v119, v137
	v_exp_f32_e32 v120, v138
	v_exp_f32_e32 v121, v139
	v_exp_f32_e32 v122, v140
	v_exp_f32_e32 v123, v141
	v_exp_f32_e32 v124, v142
	v_exp_f32_e32 v125, v143
	v_exp_f32_e32 v126, v144
.LBB0_614:
	v_exp_f32_e32 v111, v129
	v_exp_f32_e32 v127, v145
	v_cvt_pk_bf16_f32 v210, v96, v97
	v_cvt_pk_bf16_f32 v211, v98, v99
	v_cvt_pk_bf16_f32 v212, v100, v101
	v_cvt_pk_bf16_f32 v213, v102, v103
	v_cvt_pk_bf16_f32 v218, v104, v105
	v_cvt_pk_bf16_f32 v219, v106, v107
	v_cvt_pk_bf16_f32 v220, v108, v109
	v_cvt_pk_bf16_f32 v221, v110, v111
	v_cvt_pk_bf16_f32 v222, v112, v113
	v_cvt_pk_bf16_f32 v223, v114, v115
	v_cvt_pk_bf16_f32 v224, v116, v117
	v_cvt_pk_bf16_f32 v225, v118, v119
	v_cvt_pk_bf16_f32 v214, v120, v121
	v_cvt_pk_bf16_f32 v215, v122, v123
	v_cvt_pk_bf16_f32 v216, v124, v125
	v_cvt_pk_bf16_f32 v217, v126, v127
	v_permlane32_swap_b32_e32 v210, v212
	v_permlane32_swap_b32_e32 v211, v213
	v_permlane32_swap_b32_e32 v218, v220
	v_permlane32_swap_b32_e32 v219, v221
	v_permlane32_swap_b32_e32 v222, v224
	v_permlane32_swap_b32_e32 v223, v225
	v_permlane32_swap_b32_e32 v214, v216
	v_permlane32_swap_b32_e32 v215, v217
	s_and_b64 vcc, exec, s[44:45]
	s_mov_b64 s[2:3], -1
	s_cbranch_vccnz .LBB0_618
	v_exp_f32_e32 v128, v80
	v_exp_f32_e32 v129, v81
	v_exp_f32_e32 v130, v82
	v_exp_f32_e32 v131, v83
	v_exp_f32_e32 v132, v84
	v_exp_f32_e32 v133, v85
	v_exp_f32_e32 v134, v86
	v_exp_f32_e32 v135, v87
	v_exp_f32_e32 v136, v88
	v_exp_f32_e32 v137, v89
	v_exp_f32_e32 v138, v90
	v_exp_f32_e32 v139, v91
	v_exp_f32_e32 v140, v92
	v_exp_f32_e32 v141, v93
	v_exp_f32_e32 v142, v94
.LBB0_616:
	s_and_b64 vcc, exec, s[44:45]
	s_mov_b64 s[2:3], -1
	s_cbranch_vccnz .LBB0_620

.LBB0_632:
	s_and_b32 s33, s31, 1
	s_cmp_eq_u32 s90, 0xc98000
	s_movk_i32 s44, 0x4000
	s_cbranch_scc1 .LBB0_636
	s_lshl_b32 s44, s33, 14
	s_and_saveexec_b64 s[2:3], s[42:43]
	s_xor_b32 s45, s44, 0x4000
	s_add_i32 s45, s23, s45
	s_add_i32 m0, s45, 0x8000
	s_add_i32 s45, s45, 0xa000
	v_lshl_add_u64 v[66:67], v[212:213], 0, s[90:91]
	v_lshl_add_u64 v[64:65], v[214:215], 0, s[90:91]
	global_load_lds_dwordx4 v[66:67], off
	s_mov_b32 m0, s45
	s_nop 0
	global_load_lds_dwordx4 v[64:65], off

.LBB0_636:
	v_add_u32_e32 v104, s44, v221
	v_add_u32_e32 v68, v104, v222
	v_add_u32_e32 v72, v104, v223
	ds_read_b128 v[64:67], v68 offset:32768
	ds_read_b128 v[68:71], v68 offset:40960
	ds_read_b128 v[96:99], v72 offset:32768
	ds_read_b128 v[100:103], v72 offset:40960
	s_waitcnt lgkmcnt(0)
	v_mfma_f32_32x32x16_bf16 v[114:129], v[64:67], v[162:165], 0
	v_mfma_f32_32x32x16_bf16 v[80:95], v[64:67], v[178:181], 0
	v_mfma_f32_32x32x16_bf16 v[130:145], v[68:71], v[162:165], 0
	v_mfma_f32_32x32x16_bf16 v[64:79], v[68:71], v[178:181], 0
	v_mfma_f32_32x32x16_bf16 v[114:129], v[96:99], v[166:169], v[114:129]
	v_mfma_f32_32x32x16_bf16 v[80:95], v[96:99], v[182:185], v[80:95]
	v_mfma_f32_32x32x16_bf16 v[130:145], v[100:103], v[166:169], v[130:145]
	v_mfma_f32_32x32x16_bf16 v[64:79], v[100:103], v[182:185], v[64:79]
	v_add_u32_e32 v100, v104, v224
	v_add_u32_e32 v108, v104, v225
	ds_read_b128 v[96:99], v100 offset:32768
	ds_read_b128 v[100:103], v100 offset:40960
	ds_read_b128 v[104:107], v108 offset:32768
	ds_read_b128 v[108:111], v108 offset:40960
	s_waitcnt lgkmcnt(0)
	v_mfma_f32_32x32x16_bf16 v[114:129], v[96:99], v[170:173], v[114:129]
	v_mfma_f32_32x32x16_bf16 v[80:95], v[96:99], v[186:189], v[80:95]
	v_mfma_f32_32x32x16_bf16 v[130:145], v[100:103], v[170:173], v[130:145]
	v_mfma_f32_32x32x16_bf16 v[64:79], v[100:103], v[186:189], v[64:79]
	v_mfma_f32_32x32x16_bf16 v[114:129], v[104:107], v[174:177], v[114:129]
	v_mfma_f32_32x32x16_bf16 v[80:95], v[104:107], v[190:193], v[80:95]
	v_mfma_f32_32x32x16_bf16 v[130:145], v[108:111], v[174:177], v[130:145]
	v_mfma_f32_32x32x16_bf16 v[64:79], v[108:111], v[190:193], v[64:79]
	v_cndmask_b32_e64 v96, 0, 1, s[40:41]
	v_cmp_ne_u32_e64 s[44:45], 1, v96
	s_andn2_b64 vcc, exec, s[40:41]
	s_mov_b64 s[2:3], -1
	s_cbranch_vccnz .LBB0_640
	s_nop 3
	v_exp_f32_e32 v96, v114
	v_exp_f32_e32 v97, v115
	v_exp_f32_e32 v98, v116
	v_exp_f32_e32 v99, v117
	v_exp_f32_e32 v100, v118
	v_exp_f32_e32 v101, v119
	v_exp_f32_e32 v102, v120
	v_exp_f32_e32 v103, v121
	v_exp_f32_e32 v104, v122
	v_exp_f32_e32 v105, v123
	v_exp_f32_e32 v106, v124
	v_exp_f32_e32 v107, v125
	v_exp_f32_e32 v108, v126
	v_exp_f32_e32 v109, v127
	v_exp_f32_e32 v110, v128
.LBB0_638:
	s_and_b64 vcc, exec, s[44:45]
	s_mov_b64 s[2:3], -1
	s_cbranch_vccnz .LBB0_642
.LBB0_639:
	s_nop 0
	v_exp_f32_e32 v112, v130
	v_exp_f32_e32 v113, v131
	v_exp_f32_e32 v114, v132
	v_exp_f32_e32 v115, v133
	v_exp_f32_e32 v116, v134
	v_exp_f32_e32 v117, v135
	v_exp_f32_e32 v118, v136
	v_exp_f32_e32 v119, v137
	v_exp_f32_e32 v120, v138
	v_exp_f32_e32 v121, v139
	v_exp_f32_e32 v122, v140
	v_exp_f32_e32 v123, v141
	v_exp_f32_e32 v124, v142
	v_exp_f32_e32 v125, v143
	v_exp_f32_e32 v126, v144
.LBB0_644:
	v_exp_f32_e32 v111, v129
	v_exp_f32_e32 v127, v145
	v_cvt_pk_bf16_f32 v194, v96, v97
	v_cvt_pk_bf16_f32 v195, v98, v99
	v_cvt_pk_bf16_f32 v196, v100, v101
	v_cvt_pk_bf16_f32 v197, v102, v103
	v_cvt_pk_bf16_f32 v198, v104, v105
	v_cvt_pk_bf16_f32 v199, v106, v107
	v_cvt_pk_bf16_f32 v200, v108, v109
	v_cvt_pk_bf16_f32 v201, v110, v111
	v_cvt_pk_bf16_f32 v202, v112, v113
	v_cvt_pk_bf16_f32 v203, v114, v115
	v_cvt_pk_bf16_f32 v204, v116, v117
	v_cvt_pk_bf16_f32 v205, v118, v119
	v_cvt_pk_bf16_f32 v206, v120, v121
	v_cvt_pk_bf16_f32 v207, v122, v123
	v_cvt_pk_bf16_f32 v208, v124, v125
	v_cvt_pk_bf16_f32 v209, v126, v127
	v_permlane32_swap_b32_e32 v194, v196
	v_permlane32_swap_b32_e32 v195, v197
	v_permlane32_swap_b32_e32 v198, v200
	v_permlane32_swap_b32_e32 v199, v201
	v_permlane32_swap_b32_e32 v202, v204
	v_permlane32_swap_b32_e32 v203, v205
	v_permlane32_swap_b32_e32 v206, v208
	v_permlane32_swap_b32_e32 v207, v209
	s_and_b64 vcc, exec, s[44:45]
	s_mov_b64 s[2:3], -1
	s_cbranch_vccnz .LBB0_648
	v_exp_f32_e32 v128, v80
	v_exp_f32_e32 v129, v81
	v_exp_f32_e32 v130, v82
	v_exp_f32_e32 v131, v83
	v_exp_f32_e32 v132, v84
	v_exp_f32_e32 v133, v85
	v_exp_f32_e32 v134, v86
	v_exp_f32_e32 v135, v87
	v_exp_f32_e32 v136, v88
	v_exp_f32_e32 v137, v89
	v_exp_f32_e32 v138, v90
	v_exp_f32_e32 v139, v91
	v_exp_f32_e32 v140, v92
	v_exp_f32_e32 v141, v93
	v_exp_f32_e32 v142, v94
.LBB0_646:
	s_and_b64 vcc, exec, s[44:45]
	s_mov_b64 s[2:3], -1
	s_cbranch_vccnz .LBB0_650

.LBB0_663:
	ds_read_b128 v[64:67], v213 offset:32768
	ds_read_b128 v[68:71], v213 offset:40960
	ds_read_b128 v[72:75], v241 offset:32768
	ds_read_b128 v[76:79], v241 offset:40960
	ds_read_b128 v[114:117], v244 offset:32768
	ds_read_b128 v[118:121], v244 offset:40960
	ds_read_b128 v[122:125], v246 offset:32768
	ds_read_b128 v[126:129], v246 offset:40960
	s_waitcnt lgkmcnt(7)
	v_mfma_f32_32x32x16_bf16 v[82:97], v[64:67], v[162:165], 0
	s_waitcnt lgkmcnt(6)
	v_mfma_f32_32x32x16_bf16 v[98:113], v[68:71], v[162:165], 0
	s_waitcnt lgkmcnt(5)
	v_mfma_f32_32x32x16_bf16 v[82:97], v[72:75], v[166:169], v[82:97]
	s_waitcnt lgkmcnt(4)
	v_mfma_f32_32x32x16_bf16 v[98:113], v[76:79], v[166:169], v[98:113]
	s_waitcnt lgkmcnt(3)
	v_mfma_f32_32x32x16_bf16 v[82:97], v[114:117], v[170:173], v[82:97]
	s_waitcnt lgkmcnt(2)
	v_mfma_f32_32x32x16_bf16 v[98:113], v[118:121], v[170:173], v[98:113]
	s_waitcnt lgkmcnt(1)
	v_mfma_f32_32x32x16_bf16 v[82:97], v[122:125], v[174:177], v[82:97]
	s_waitcnt lgkmcnt(0)
	v_mfma_f32_32x32x16_bf16 v[98:113], v[126:129], v[174:177], v[98:113]
	ds_read_b128 v[64:67], v247 offset:32768
	ds_read_b128 v[68:71], v247 offset:40960
	ds_read_b128 v[72:75], v249 offset:32768
	ds_read_b128 v[76:79], v249 offset:40960
	ds_read_b128 v[114:117], v226 offset:32768
	ds_read_b128 v[118:121], v226 offset:40960
	ds_read_b128 v[122:125], v227 offset:32768
	ds_read_b128 v[126:129], v227 offset:40960
	s_waitcnt lgkmcnt(7)
	v_mfma_f32_32x32x16_bf16 v[82:97], v[64:67], v[178:181], v[82:97]
	s_waitcnt lgkmcnt(6)
	v_mfma_f32_32x32x16_bf16 v[98:113], v[68:71], v[178:181], v[98:113]
	s_waitcnt lgkmcnt(5)
	v_mfma_f32_32x32x16_bf16 v[82:97], v[72:75], v[182:185], v[82:97]
	s_waitcnt lgkmcnt(4)
	v_mfma_f32_32x32x16_bf16 v[98:113], v[76:79], v[182:185], v[98:113]
	s_waitcnt lgkmcnt(3)
	v_mfma_f32_32x32x16_bf16 v[82:97], v[114:117], v[186:189], v[82:97]
	s_waitcnt lgkmcnt(2)
	v_mfma_f32_32x32x16_bf16 v[98:113], v[118:121], v[186:189], v[98:113]
	s_waitcnt lgkmcnt(1)
	v_mfma_f32_32x32x16_bf16 v[82:97], v[122:125], v[190:193], v[82:97]
	s_waitcnt lgkmcnt(0)
	v_mfma_f32_32x32x16_bf16 v[98:113], v[126:129], v[190:193], v[98:113]
	s_barrier
	v_cndmask_b32_e64 v64, 0, 1, s[40:41]
	v_cmp_ne_u32_e64 s[42:43], 1, v64
	s_andn2_b64 vcc, exec, s[40:41]
	s_mov_b64 s[2:3], -1
	s_cbranch_vccnz .LBB0_667
	s_nop 3
	v_exp_f32_e32 v64, v82
	v_exp_f32_e32 v65, v83
	v_exp_f32_e32 v66, v84
	v_exp_f32_e32 v67, v85
	v_exp_f32_e32 v68, v86
	v_exp_f32_e32 v69, v87
	v_exp_f32_e32 v70, v88
	v_exp_f32_e32 v71, v89
	v_exp_f32_e32 v72, v90
	v_exp_f32_e32 v73, v91
	v_exp_f32_e32 v74, v92
	v_exp_f32_e32 v75, v93
	v_exp_f32_e32 v76, v94
	v_exp_f32_e32 v77, v95
	v_exp_f32_e32 v78, v96
.LBB0_665:
	s_and_b64 vcc, exec, s[42:43]
	s_mov_b64 s[2:3], -1
	s_cbranch_vccnz .LBB0_669
.LBB0_666:
	s_nop 0
	v_exp_f32_e32 v80, v98
	v_exp_f32_e32 v81, v99
	v_exp_f32_e32 v82, v100
	v_exp_f32_e32 v83, v101
	v_exp_f32_e32 v84, v102
	v_exp_f32_e32 v85, v103
	v_exp_f32_e32 v86, v104
	v_exp_f32_e32 v87, v105
	v_exp_f32_e32 v88, v106
	v_exp_f32_e32 v89, v107
	v_exp_f32_e32 v90, v108
	v_exp_f32_e32 v91, v109
	v_exp_f32_e32 v92, v110
	v_exp_f32_e32 v93, v111
	v_exp_f32_e32 v94, v112
.LBB0_671:
	v_exp_f32_e32 v79, v97
	v_exp_f32_e32 v95, v113
	v_cvt_pk_bf16_f32 v96, v64, v65
	v_cvt_pk_bf16_f32 v97, v66, v67
	v_cvt_pk_bf16_f32 v98, v68, v69
	v_cvt_pk_bf16_f32 v99, v70, v71
	v_cvt_pk_bf16_f32 v100, v72, v73
	v_cvt_pk_bf16_f32 v101, v74, v75
	v_cvt_pk_bf16_f32 v102, v76, v77
	v_cvt_pk_bf16_f32 v103, v78, v79
	v_cvt_pk_bf16_f32 v104, v80, v81
	v_cvt_pk_bf16_f32 v105, v82, v83
	v_cvt_pk_bf16_f32 v106, v84, v85
	v_cvt_pk_bf16_f32 v107, v86, v87
	v_cvt_pk_bf16_f32 v108, v88, v89
	v_cvt_pk_bf16_f32 v109, v90, v91
	v_cvt_pk_bf16_f32 v110, v92, v93
	v_cvt_pk_bf16_f32 v111, v94, v95
	v_permlane32_swap_b32_e32 v96, v98
	v_permlane32_swap_b32_e32 v97, v99
	v_permlane32_swap_b32_e32 v100, v102
	v_permlane32_swap_b32_e32 v101, v103
	v_permlane32_swap_b32_e32 v104, v106
	v_permlane32_swap_b32_e32 v105, v107
	v_permlane32_swap_b32_e32 v108, v110
	v_permlane32_swap_b32_e32 v109, v111
	s_waitcnt vmcnt(0)
	v_cndmask_b32_e64 v112, 0, 1, s[48:49]
	v_cmp_ne_u32_e64 s[44:45], 1, v112
	s_andn2_b64 vcc, exec, s[48:49]
	s_waitcnt vmcnt(3)
	ds_write_b128 v232, v[194:197] offset:49152
	s_waitcnt vmcnt(1)
	ds_write_b128 v233, v[202:205] offset:49152
	ds_write_b128 v234, v[198:201] offset:16384
	s_waitcnt vmcnt(0)
	ds_write_b128 v235, v[206:209] offset:16384
	s_waitcnt lgkmcnt(0)
	s_barrier
	s_cbranch_vccnz .LBB0_673
	global_load_dwordx4 v[194:197], v[214:215], off
	global_load_dwordx4 v[202:205], v[216:217], off
	global_load_dwordx4 v[198:201], v[218:219], off
	global_load_dwordx4 v[206:209], v[220:221], off
.LBB0_673:
	ds_read_b64_tr_b16 v[112:113], v231 offset:0
	ds_read_b64_tr_b16 v[114:115], v231 offset:0x800
	ds_read_b64_tr_b16 v[116:117], v231 offset:0x1000
	ds_read_b64_tr_b16 v[118:119], v231 offset:0x1800
	ds_read_b64_tr_b16 v[120:121], v231 offset:0x2000
	ds_read_b64_tr_b16 v[122:123], v231 offset:0x2800
	ds_read_b64_tr_b16 v[124:125], v231 offset:0x3000
	ds_read_b64_tr_b16 v[126:127], v231 offset:0x3800
	s_waitcnt lgkmcnt(0)
	s_nop 0
	v_mfma_f32_32x32x16_bf16 v[0:15], v[96:99], v[112:115], v[0:15]
	ds_read_b64_tr_b16 v[112:113], v231 offset:0x200
	ds_read_b64_tr_b16 v[114:115], v231 offset:0xa00
	v_mfma_f32_32x32x16_bf16 v[0:15], v[100:103], v[116:119], v[0:15]
	ds_read_b64_tr_b16 v[116:117], v231 offset:0x1200
	ds_read_b64_tr_b16 v[118:119], v231 offset:0x1a00
	v_mfma_f32_32x32x16_bf16 v[0:15], v[104:107], v[120:123], v[0:15]
	ds_read_b64_tr_b16 v[120:121], v231 offset:0x2200
	ds_read_b64_tr_b16 v[122:123], v231 offset:0x2a00
	v_mfma_f32_32x32x16_bf16 v[0:15], v[108:111], v[124:127], v[0:15]
	ds_read_b64_tr_b16 v[124:125], v231 offset:0x3200
	ds_read_b64_tr_b16 v[126:127], v231 offset:0x3a00
	s_waitcnt lgkmcnt(0)
	v_mfma_f32_32x32x16_bf16 v[16:31], v[96:99], v[112:115], v[16:31]
	ds_read_b64_tr_b16 v[112:113], v231 offset:0x400
	ds_read_b64_tr_b16 v[114:115], v231 offset:0xc00
	v_mfma_f32_32x32x16_bf16 v[16:31], v[100:103], v[116:119], v[16:31]
	ds_read_b64_tr_b16 v[116:117], v231 offset:0x1400
	ds_read_b64_tr_b16 v[118:119], v231 offset:0x1c00
	v_mfma_f32_32x32x16_bf16 v[16:31], v[104:107], v[120:123], v[16:31]
	ds_read_b64_tr_b16 v[120:121], v231 offset:0x2400
	ds_read_b64_tr_b16 v[122:123], v231 offset:0x2c00
	v_mfma_f32_32x32x16_bf16 v[16:31], v[108:111], v[124:127], v[16:31]
	ds_read_b64_tr_b16 v[124:125], v231 offset:0x3400
	ds_read_b64_tr_b16 v[126:127], v231 offset:0x3c00
	s_waitcnt lgkmcnt(0)
	v_mfma_f32_32x32x16_bf16 v[32:47], v[96:99], v[112:115], v[32:47]
	ds_read_b64_tr_b16 v[112:113], v231 offset:0x600
	ds_read_b64_tr_b16 v[114:115], v231 offset:0xe00
	v_mfma_f32_32x32x16_bf16 v[32:47], v[100:103], v[116:119], v[32:47]
	ds_read_b64_tr_b16 v[116:117], v231 offset:0x1600
	ds_read_b64_tr_b16 v[118:119], v231 offset:0x1e00
	v_mfma_f32_32x32x16_bf16 v[32:47], v[104:107], v[120:123], v[32:47]
	ds_read_b64_tr_b16 v[120:121], v231 offset:0x2600
	ds_read_b64_tr_b16 v[122:123], v231 offset:0x2e00
	v_mfma_f32_32x32x16_bf16 v[32:47], v[108:111], v[124:127], v[32:47]
	ds_read_b64_tr_b16 v[124:125], v231 offset:0x3600
	ds_read_b64_tr_b16 v[126:127], v231 offset:0x3e00
	s_waitcnt lgkmcnt(0)
	v_mfma_f32_32x32x16_bf16 v[48:63], v[96:99], v[112:115], v[48:63]
	v_mfma_f32_32x32x16_bf16 v[48:63], v[100:103], v[116:119], v[48:63]
	v_mfma_f32_32x32x16_bf16 v[48:63], v[104:107], v[120:123], v[48:63]
	v_mfma_f32_32x32x16_bf16 v[48:63], v[108:111], v[124:127], v[48:63]
	ds_read_b128 v[96:99], v213 offset:49152
	ds_read_b128 v[100:103], v213 offset:57344
	ds_read_b128 v[104:107], v241 offset:49152
	ds_read_b128 v[108:111], v241 offset:57344
	ds_read_b128 v[144:147], v244 offset:49152
	ds_read_b128 v[148:151], v244 offset:57344
	ds_read_b128 v[152:155], v246 offset:49152
	ds_read_b128 v[156:159], v246 offset:57344
	s_waitcnt lgkmcnt(7)
	v_mfma_f32_32x32x16_bf16 v[112:127], v[96:99], v[162:165], 0
	s_waitcnt lgkmcnt(6)
	v_mfma_f32_32x32x16_bf16 v[128:143], v[100:103], v[162:165], 0
	s_waitcnt lgkmcnt(5)
	v_mfma_f32_32x32x16_bf16 v[112:127], v[104:107], v[166:169], v[112:127]
	s_waitcnt lgkmcnt(4)
	v_mfma_f32_32x32x16_bf16 v[128:143], v[108:111], v[166:169], v[128:143]
	s_waitcnt lgkmcnt(3)
	v_mfma_f32_32x32x16_bf16 v[112:127], v[144:147], v[170:173], v[112:127]
	s_waitcnt lgkmcnt(2)
	v_mfma_f32_32x32x16_bf16 v[128:143], v[148:151], v[170:173], v[128:143]
	s_waitcnt lgkmcnt(1)
	v_mfma_f32_32x32x16_bf16 v[112:127], v[152:155], v[174:177], v[112:127]
	s_waitcnt lgkmcnt(0)
	v_mfma_f32_32x32x16_bf16 v[128:143], v[156:159], v[174:177], v[128:143]
	ds_read_b128 v[96:99], v247 offset:49152
	ds_read_b128 v[100:103], v247 offset:57344
	ds_read_b128 v[104:107], v249 offset:49152
	ds_read_b128 v[108:111], v249 offset:57344
	ds_read_b128 v[144:147], v226 offset:49152
	ds_read_b128 v[148:151], v226 offset:57344
	ds_read_b128 v[152:155], v227 offset:49152
	ds_read_b128 v[156:159], v227 offset:57344
	s_waitcnt lgkmcnt(7)
	v_mfma_f32_32x32x16_bf16 v[112:127], v[96:99], v[178:181], v[112:127]
	s_waitcnt lgkmcnt(6)
	v_mfma_f32_32x32x16_bf16 v[128:143], v[100:103], v[178:181], v[128:143]
	s_waitcnt lgkmcnt(5)
	v_mfma_f32_32x32x16_bf16 v[112:127], v[104:107], v[182:185], v[112:127]
	s_waitcnt lgkmcnt(4)
	v_mfma_f32_32x32x16_bf16 v[128:143], v[108:111], v[182:185], v[128:143]
	s_waitcnt lgkmcnt(3)
	v_mfma_f32_32x32x16_bf16 v[112:127], v[144:147], v[186:189], v[112:127]
	s_waitcnt lgkmcnt(2)
	v_mfma_f32_32x32x16_bf16 v[128:143], v[148:151], v[186:189], v[128:143]
	s_waitcnt lgkmcnt(1)
	v_mfma_f32_32x32x16_bf16 v[112:127], v[152:155], v[190:193], v[112:127]
	s_waitcnt lgkmcnt(0)
	v_mfma_f32_32x32x16_bf16 v[128:143], v[156:159], v[190:193], v[128:143]
	s_barrier
	s_and_b64 vcc, exec, s[42:43]
	s_mov_b64 s[2:3], -1
	s_cbranch_vccnz .LBB0_677
	s_nop 5
	v_exp_f32_e32 v96, v112
	v_exp_f32_e32 v97, v113
	v_exp_f32_e32 v98, v114
	v_exp_f32_e32 v99, v115
	v_exp_f32_e32 v100, v116
	v_exp_f32_e32 v101, v117
	v_exp_f32_e32 v102, v118
	v_exp_f32_e32 v103, v119
	v_exp_f32_e32 v104, v120
	v_exp_f32_e32 v105, v121
	v_exp_f32_e32 v106, v122
	v_exp_f32_e32 v107, v123
	v_exp_f32_e32 v108, v124
	v_exp_f32_e32 v109, v125
	v_exp_f32_e32 v110, v126
.LBB0_675:
	s_and_b64 vcc, exec, s[42:43]
	s_mov_b64 s[2:3], -1
	s_cbranch_vccnz .LBB0_679
.LBB0_676:
	s_nop 2
	v_exp_f32_e32 v144, v128
	v_exp_f32_e32 v145, v129
	v_exp_f32_e32 v146, v130
	v_exp_f32_e32 v147, v131
	v_exp_f32_e32 v148, v132
	v_exp_f32_e32 v149, v133
	v_exp_f32_e32 v150, v134
	v_exp_f32_e32 v151, v135
	v_exp_f32_e32 v152, v136
	v_exp_f32_e32 v153, v137
	v_exp_f32_e32 v154, v138
	v_exp_f32_e32 v155, v139
	v_exp_f32_e32 v156, v140
	v_exp_f32_e32 v157, v141
	v_exp_f32_e32 v158, v142
.LBB0_681:
	v_exp_f32_e32 v111, v127
	v_exp_f32_e32 v159, v143
	v_cvt_pk_bf16_f32 v124, v96, v97
	v_cvt_pk_bf16_f32 v125, v98, v99
	v_cvt_pk_bf16_f32 v126, v100, v101
	v_cvt_pk_bf16_f32 v127, v102, v103
	v_cvt_pk_bf16_f32 v120, v104, v105
	v_cvt_pk_bf16_f32 v121, v106, v107
	v_cvt_pk_bf16_f32 v122, v108, v109
	v_cvt_pk_bf16_f32 v123, v110, v111
	v_cvt_pk_bf16_f32 v116, v144, v145
	v_cvt_pk_bf16_f32 v117, v146, v147
	v_cvt_pk_bf16_f32 v118, v148, v149
	v_cvt_pk_bf16_f32 v119, v150, v151
	v_cvt_pk_bf16_f32 v112, v152, v153
	v_cvt_pk_bf16_f32 v113, v154, v155
	v_cvt_pk_bf16_f32 v114, v156, v157
	v_cvt_pk_bf16_f32 v115, v158, v159
	v_permlane32_swap_b32_e32 v124, v126
	v_permlane32_swap_b32_e32 v125, v127
	v_permlane32_swap_b32_e32 v120, v122
	v_permlane32_swap_b32_e32 v121, v123
	v_permlane32_swap_b32_e32 v116, v118
	v_permlane32_swap_b32_e32 v117, v119
	v_permlane32_swap_b32_e32 v112, v114
	v_permlane32_swap_b32_e32 v113, v115
	s_and_b64 vcc, exec, s[44:45]
	s_cbranch_vccnz .LBB0_660
	s_waitcnt vmcnt(0)
	s_waitcnt vmcnt(3)
	ds_write_b128 v232, v[194:197] offset:32768
	s_waitcnt vmcnt(2)
	ds_write_b128 v233, v[202:205] offset:32768
	s_waitcnt vmcnt(1)
	ds_write_b128 v234, v[198:201]
	s_waitcnt vmcnt(0)
	ds_write_b128 v235, v[206:209]
	s_branch .LBB0_660

.LBB0_687:
	s_lshl_b64 s[2:3], s[2:3], 1
	s_add_u32 s2, s18, s2
	s_addc_u32 s3, s19, s3
	global_load_dwordx4 v[146:149], v210, s[2:3]
	global_load_dwordx4 v[150:153], v210, s[2:3] offset:256
	global_load_dwordx4 v[154:157], v212, s[2:3]
	global_load_dwordx4 v[194:197], v212, s[2:3] offset:256
	ds_read_b128 v[64:67], v204 offset:32768
	ds_read_b128 v[68:71], v204 offset:40960
	ds_read_b128 v[72:75], v205 offset:32768
	ds_read_b128 v[76:79], v205 offset:40960
	ds_read_b128 v[80:83], v206 offset:32768
	ds_read_b128 v[84:87], v206 offset:40960
	ds_read_b128 v[88:91], v207 offset:32768
	ds_read_b128 v[92:95], v207 offset:40960
	s_waitcnt lgkmcnt(7)
	v_mfma_f32_32x32x16_bf16 v[112:127], v[64:67], v[162:165], 0
	s_waitcnt lgkmcnt(6)
	v_mfma_f32_32x32x16_bf16 v[96:111], v[68:71], v[162:165], 0
	s_waitcnt lgkmcnt(5)
	v_mfma_f32_32x32x16_bf16 v[112:127], v[72:75], v[166:169], v[112:127]
	s_waitcnt lgkmcnt(4)
	v_mfma_f32_32x32x16_bf16 v[96:111], v[76:79], v[166:169], v[96:111]
	s_waitcnt lgkmcnt(3)
	v_mfma_f32_32x32x16_bf16 v[112:127], v[80:83], v[170:173], v[112:127]
	s_waitcnt lgkmcnt(2)
	v_mfma_f32_32x32x16_bf16 v[96:111], v[84:87], v[170:173], v[96:111]
	s_waitcnt lgkmcnt(1)
	v_mfma_f32_32x32x16_bf16 v[112:127], v[88:91], v[174:177], v[112:127]
	s_waitcnt lgkmcnt(0)
	v_mfma_f32_32x32x16_bf16 v[96:111], v[92:95], v[174:177], v[96:111]
	ds_read_b128 v[64:67], v208 offset:32768
	ds_read_b128 v[68:71], v208 offset:40960
	ds_read_b128 v[72:75], v209 offset:32768
	ds_read_b128 v[76:79], v209 offset:40960
	ds_read_b128 v[80:83], v213 offset:32768
	ds_read_b128 v[84:87], v213 offset:40960
	ds_read_b128 v[88:91], v214 offset:32768
	ds_read_b128 v[92:95], v214 offset:40960
	s_waitcnt lgkmcnt(7)
	v_mfma_f32_32x32x16_bf16 v[112:127], v[64:67], v[178:181], v[112:127]
	s_waitcnt lgkmcnt(6)
	v_mfma_f32_32x32x16_bf16 v[96:111], v[68:71], v[178:181], v[96:111]
	s_waitcnt lgkmcnt(5)
	v_mfma_f32_32x32x16_bf16 v[112:127], v[72:75], v[182:185], v[112:127]
	s_waitcnt lgkmcnt(4)
	v_mfma_f32_32x32x16_bf16 v[96:111], v[76:79], v[182:185], v[96:111]
	s_waitcnt lgkmcnt(3)
	v_mfma_f32_32x32x16_bf16 v[112:127], v[80:83], v[186:189], v[112:127]
	s_waitcnt lgkmcnt(2)
	v_mfma_f32_32x32x16_bf16 v[96:111], v[84:87], v[186:189], v[96:111]
	s_waitcnt lgkmcnt(1)
	v_mfma_f32_32x32x16_bf16 v[112:127], v[88:91], v[190:193], v[112:127]
	s_waitcnt lgkmcnt(0)
	v_mfma_f32_32x32x16_bf16 v[96:111], v[92:95], v[190:193], v[96:111]
	v_cndmask_b32_e64 v64, 0, 1, s[40:41]
	v_cmp_ne_u32_e64 s[42:43], 1, v64
	s_andn2_b64 vcc, exec, s[40:41]
	s_mov_b64 s[2:3], -1
	s_cbranch_vccnz .LBB0_691
	s_nop 4
	v_exp_f32_e32 v64, v112
	v_exp_f32_e32 v65, v113
	v_exp_f32_e32 v66, v114
	v_exp_f32_e32 v67, v115
	v_exp_f32_e32 v68, v116
	v_exp_f32_e32 v69, v117
	v_exp_f32_e32 v70, v118
	v_exp_f32_e32 v71, v119
	v_exp_f32_e32 v72, v120
	v_exp_f32_e32 v73, v121
	v_exp_f32_e32 v74, v122
	v_exp_f32_e32 v75, v123
	v_exp_f32_e32 v76, v124
	v_exp_f32_e32 v77, v125
	v_exp_f32_e32 v78, v126
.LBB0_689:
	s_and_b64 vcc, exec, s[42:43]
	s_mov_b64 s[2:3], -1
	s_cbranch_vccnz .LBB0_693
.LBB0_690:
	s_nop 1
	v_exp_f32_e32 v80, v96
	v_exp_f32_e32 v81, v97
	v_exp_f32_e32 v82, v98
	v_exp_f32_e32 v83, v99
	v_exp_f32_e32 v84, v100
	v_exp_f32_e32 v85, v101
	v_exp_f32_e32 v86, v102
	v_exp_f32_e32 v87, v103
	v_exp_f32_e32 v88, v104
	v_exp_f32_e32 v89, v105
	v_exp_f32_e32 v90, v106
	v_exp_f32_e32 v91, v107
	v_exp_f32_e32 v92, v108
	v_exp_f32_e32 v93, v109
	v_exp_f32_e32 v94, v110
.LBB0_695:
	v_exp_f32_e32 v79, v127
	v_exp_f32_e32 v95, v111
	v_cvt_pk_bf16_f32 v96, v64, v65
	v_cvt_pk_bf16_f32 v97, v66, v67
	v_cvt_pk_bf16_f32 v98, v68, v69
	v_cvt_pk_bf16_f32 v99, v70, v71
	v_cvt_pk_bf16_f32 v100, v72, v73
	v_cvt_pk_bf16_f32 v101, v74, v75
	v_cvt_pk_bf16_f32 v102, v76, v77
	v_cvt_pk_bf16_f32 v103, v78, v79
	v_cvt_pk_bf16_f32 v104, v80, v81
	v_cvt_pk_bf16_f32 v105, v82, v83
	v_cvt_pk_bf16_f32 v106, v84, v85
	v_cvt_pk_bf16_f32 v107, v86, v87
	v_cvt_pk_bf16_f32 v108, v88, v89
	v_cvt_pk_bf16_f32 v109, v90, v91
	v_cvt_pk_bf16_f32 v110, v92, v93
	v_cvt_pk_bf16_f32 v111, v94, v95
	v_permlane32_swap_b32_e32 v96, v98
	v_permlane32_swap_b32_e32 v97, v99
	v_permlane32_swap_b32_e32 v100, v102
	v_permlane32_swap_b32_e32 v101, v103
	v_permlane32_swap_b32_e32 v104, v106
	v_permlane32_swap_b32_e32 v105, v107
	v_permlane32_swap_b32_e32 v108, v110
	v_permlane32_swap_b32_e32 v109, v111
	s_barrier
	ds_read_b64_tr_b16 v[112:113], v231 offset:0
	ds_read_b64_tr_b16 v[114:115], v231 offset:0x800
	ds_read_b64_tr_b16 v[116:117], v231 offset:0x1000
	ds_read_b64_tr_b16 v[118:119], v231 offset:0x1800
	ds_read_b64_tr_b16 v[120:121], v231 offset:0x2000
	ds_read_b64_tr_b16 v[122:123], v231 offset:0x2800
	ds_read_b64_tr_b16 v[124:125], v231 offset:0x3000
	ds_read_b64_tr_b16 v[126:127], v231 offset:0x3800
	s_waitcnt lgkmcnt(0)
	s_nop 0
	v_mfma_f32_32x32x16_bf16 v[0:15], v[96:99], v[112:115], v[0:15]
	ds_read_b64_tr_b16 v[112:113], v231 offset:0x200
	ds_read_b64_tr_b16 v[114:115], v231 offset:0xa00
	v_mfma_f32_32x32x16_bf16 v[0:15], v[100:103], v[116:119], v[0:15]
	ds_read_b64_tr_b16 v[116:117], v231 offset:0x1200
	ds_read_b64_tr_b16 v[118:119], v231 offset:0x1a00
	v_mfma_f32_32x32x16_bf16 v[0:15], v[104:107], v[120:123], v[0:15]
	ds_read_b64_tr_b16 v[120:121], v231 offset:0x2200
	ds_read_b64_tr_b16 v[122:123], v231 offset:0x2a00
	v_mfma_f32_32x32x16_bf16 v[0:15], v[108:111], v[124:127], v[0:15]
	ds_read_b64_tr_b16 v[124:125], v231 offset:0x3200
	ds_read_b64_tr_b16 v[126:127], v231 offset:0x3a00
	s_waitcnt lgkmcnt(0)
	v_mfma_f32_32x32x16_bf16 v[16:31], v[96:99], v[112:115], v[16:31]
	ds_read_b64_tr_b16 v[112:113], v231 offset:0x400
	ds_read_b64_tr_b16 v[114:115], v231 offset:0xc00
	v_mfma_f32_32x32x16_bf16 v[16:31], v[100:103], v[116:119], v[16:31]
	ds_read_b64_tr_b16 v[116:117], v231 offset:0x1400
	ds_read_b64_tr_b16 v[118:119], v231 offset:0x1c00
	v_mfma_f32_32x32x16_bf16 v[16:31], v[104:107], v[120:123], v[16:31]
	ds_read_b64_tr_b16 v[120:121], v231 offset:0x2400
	ds_read_b64_tr_b16 v[122:123], v231 offset:0x2c00
	v_mfma_f32_32x32x16_bf16 v[16:31], v[108:111], v[124:127], v[16:31]
	ds_read_b64_tr_b16 v[124:125], v231 offset:0x3400
	ds_read_b64_tr_b16 v[126:127], v231 offset:0x3c00
	s_waitcnt lgkmcnt(0)
	v_mfma_f32_32x32x16_bf16 v[32:47], v[96:99], v[112:115], v[32:47]
	ds_read_b64_tr_b16 v[112:113], v231 offset:0x600
	ds_read_b64_tr_b16 v[114:115], v231 offset:0xe00
	v_mfma_f32_32x32x16_bf16 v[32:47], v[100:103], v[116:119], v[32:47]
	ds_read_b64_tr_b16 v[116:117], v231 offset:0x1600
	ds_read_b64_tr_b16 v[118:119], v231 offset:0x1e00
	v_mfma_f32_32x32x16_bf16 v[32:47], v[104:107], v[120:123], v[32:47]
	ds_read_b64_tr_b16 v[120:121], v231 offset:0x2600
	ds_read_b64_tr_b16 v[122:123], v231 offset:0x2e00
	v_mfma_f32_32x32x16_bf16 v[32:47], v[108:111], v[124:127], v[32:47]
	ds_read_b64_tr_b16 v[124:125], v231 offset:0x3600
	ds_read_b64_tr_b16 v[126:127], v231 offset:0x3e00
	s_waitcnt lgkmcnt(0)
	v_mfma_f32_32x32x16_bf16 v[48:63], v[96:99], v[112:115], v[48:63]
	s_waitcnt vmcnt(0)
	v_cndmask_b32_e64 v96, 0, 1, s[48:49]
	v_cmp_ne_u32_e64 s[44:45], 1, v96
	s_andn2_b64 vcc, exec, s[48:49]
	s_waitcnt vmcnt(3)
	ds_write_b128 v232, v[146:149] offset:49152
	s_waitcnt vmcnt(1)
	ds_write_b128 v233, v[154:157] offset:49152
	ds_write_b128 v234, v[150:153] offset:16384
	s_waitcnt vmcnt(0)
	ds_write_b128 v235, v[194:197] offset:16384
	s_waitcnt lgkmcnt(0)
	v_mfma_f32_32x32x16_bf16 v[48:63], v[100:103], v[116:119], v[48:63]
	s_barrier
	v_mfma_f32_32x32x16_bf16 v[48:63], v[104:107], v[120:123], v[48:63]
	v_mfma_f32_32x32x16_bf16 v[48:63], v[108:111], v[124:127], v[48:63]
	s_cbranch_vccnz .LBB0_697
	global_load_dwordx4 v[146:149], v[158:159], off
	global_load_dwordx4 v[154:157], v[198:199], off
	global_load_dwordx4 v[150:153], v[200:201], off
	global_load_dwordx4 v[194:197], v[202:203], off
.LBB0_697:
	ds_read_b128 v[96:99], v204 offset:49152
	ds_read_b128 v[100:103], v204 offset:57344
	ds_read_b128 v[104:107], v205 offset:49152
	ds_read_b128 v[108:111], v205 offset:57344
	ds_read_b128 v[216:219], v206 offset:49152
	ds_read_b128 v[226:229], v206 offset:57344
	ds_read_b128 v[236:239], v207 offset:49152
	ds_read_b128 v[246:249], v207 offset:57344
	s_waitcnt lgkmcnt(7)
	v_mfma_f32_32x32x16_bf16 v[114:129], v[96:99], v[162:165], 0
	s_waitcnt lgkmcnt(6)
	v_mfma_f32_32x32x16_bf16 v[130:145], v[100:103], v[162:165], 0
	s_waitcnt lgkmcnt(5)
	v_mfma_f32_32x32x16_bf16 v[114:129], v[104:107], v[166:169], v[114:129]
	s_waitcnt lgkmcnt(4)
	v_mfma_f32_32x32x16_bf16 v[130:145], v[108:111], v[166:169], v[130:145]
	s_waitcnt lgkmcnt(3)
	v_mfma_f32_32x32x16_bf16 v[114:129], v[216:219], v[170:173], v[114:129]
	s_waitcnt lgkmcnt(2)
	v_mfma_f32_32x32x16_bf16 v[130:145], v[226:229], v[170:173], v[130:145]
	s_waitcnt lgkmcnt(1)
	v_mfma_f32_32x32x16_bf16 v[114:129], v[236:239], v[174:177], v[114:129]
	s_waitcnt lgkmcnt(0)
	v_mfma_f32_32x32x16_bf16 v[130:145], v[246:249], v[174:177], v[130:145]
	ds_read_b128 v[96:99], v208 offset:49152
	ds_read_b128 v[100:103], v208 offset:57344
	ds_read_b128 v[104:107], v209 offset:49152
	ds_read_b128 v[108:111], v209 offset:57344
	ds_read_b128 v[216:219], v213 offset:49152
	ds_read_b128 v[226:229], v213 offset:57344
	ds_read_b128 v[236:239], v214 offset:49152
	ds_read_b128 v[246:249], v214 offset:57344
	s_waitcnt lgkmcnt(7)
	v_mfma_f32_32x32x16_bf16 v[114:129], v[96:99], v[178:181], v[114:129]
	s_waitcnt lgkmcnt(6)
	v_mfma_f32_32x32x16_bf16 v[130:145], v[100:103], v[178:181], v[130:145]
	s_waitcnt lgkmcnt(5)
	v_mfma_f32_32x32x16_bf16 v[114:129], v[104:107], v[182:185], v[114:129]
	s_waitcnt lgkmcnt(4)
	v_mfma_f32_32x32x16_bf16 v[130:145], v[108:111], v[182:185], v[130:145]
	s_waitcnt lgkmcnt(3)
	v_mfma_f32_32x32x16_bf16 v[114:129], v[216:219], v[186:189], v[114:129]
	s_waitcnt lgkmcnt(2)
	v_mfma_f32_32x32x16_bf16 v[130:145], v[226:229], v[186:189], v[130:145]
	s_waitcnt lgkmcnt(1)
	v_mfma_f32_32x32x16_bf16 v[114:129], v[236:239], v[190:193], v[114:129]
	s_waitcnt lgkmcnt(0)
	v_mfma_f32_32x32x16_bf16 v[130:145], v[246:249], v[190:193], v[130:145]
	s_and_b64 vcc, exec, s[42:43]
	s_mov_b64 s[2:3], -1
	s_cbranch_vccnz .LBB0_701
	s_nop 6
	v_exp_f32_e32 v96, v114
	v_exp_f32_e32 v97, v115
	v_exp_f32_e32 v98, v116
	v_exp_f32_e32 v99, v117
	v_exp_f32_e32 v100, v118
	v_exp_f32_e32 v101, v119
	v_exp_f32_e32 v102, v120
	v_exp_f32_e32 v103, v121
	v_exp_f32_e32 v104, v122
	v_exp_f32_e32 v105, v123
	v_exp_f32_e32 v106, v124
	v_exp_f32_e32 v107, v125
	v_exp_f32_e32 v108, v126
	v_exp_f32_e32 v109, v127
	v_exp_f32_e32 v110, v128
.LBB0_699:
	s_and_b64 vcc, exec, s[42:43]
	s_mov_b64 s[2:3], -1
	s_cbranch_vccnz .LBB0_703
.LBB0_700:
	s_nop 3
	v_exp_f32_e32 v112, v130
	v_exp_f32_e32 v113, v131
	v_exp_f32_e32 v114, v132
	v_exp_f32_e32 v115, v133
	v_exp_f32_e32 v116, v134
	v_exp_f32_e32 v117, v135
	v_exp_f32_e32 v118, v136
	v_exp_f32_e32 v119, v137
	v_exp_f32_e32 v120, v138
	v_exp_f32_e32 v121, v139
	v_exp_f32_e32 v122, v140
	v_exp_f32_e32 v123, v141
	v_exp_f32_e32 v124, v142
	v_exp_f32_e32 v125, v143
	v_exp_f32_e32 v126, v144
.LBB0_705:
	v_exp_f32_e32 v111, v129
	s_nop 0
	v_exp_f32_e32 v127, v145
	v_cvt_pk_bf16_f32 v128, v96, v97
	v_cvt_pk_bf16_f32 v129, v98, v99
	v_cvt_pk_bf16_f32 v130, v100, v101
	v_cvt_pk_bf16_f32 v131, v102, v103
	v_cvt_pk_bf16_f32 v132, v104, v105
	v_cvt_pk_bf16_f32 v133, v106, v107
	v_cvt_pk_bf16_f32 v134, v108, v109
	v_cvt_pk_bf16_f32 v135, v110, v111
	v_cvt_pk_bf16_f32 v136, v112, v113
	v_cvt_pk_bf16_f32 v137, v114, v115
	v_cvt_pk_bf16_f32 v138, v116, v117
	v_cvt_pk_bf16_f32 v139, v118, v119
	v_cvt_pk_bf16_f32 v140, v120, v121
	v_cvt_pk_bf16_f32 v141, v122, v123
	v_cvt_pk_bf16_f32 v142, v124, v125
	v_cvt_pk_bf16_f32 v143, v126, v127
	v_permlane32_swap_b32_e32 v128, v130
	v_permlane32_swap_b32_e32 v129, v131
	v_permlane32_swap_b32_e32 v132, v134
	v_permlane32_swap_b32_e32 v133, v135
	v_permlane32_swap_b32_e32 v136, v138
	v_permlane32_swap_b32_e32 v137, v139
	v_permlane32_swap_b32_e32 v140, v142
	v_permlane32_swap_b32_e32 v141, v143
	s_barrier
	ds_read_b64_tr_b16 v[216:217], v160 offset:0
	ds_read_b64_tr_b16 v[218:219], v160 offset:0x800
	ds_read_b64_tr_b16 v[226:227], v160 offset:0x1000
	ds_read_b64_tr_b16 v[228:229], v160 offset:0x1800
	ds_read_b64_tr_b16 v[236:237], v160 offset:0x2000
	ds_read_b64_tr_b16 v[238:239], v160 offset:0x2800
	ds_read_b64_tr_b16 v[246:247], v160 offset:0x3000
	ds_read_b64_tr_b16 v[248:249], v160 offset:0x3800
	s_waitcnt lgkmcnt(0)
	s_nop 0
	v_mfma_f32_32x32x16_bf16 v[0:15], v[128:131], v[216:219], v[0:15]
	ds_read_b64_tr_b16 v[216:217], v160 offset:0x200
	ds_read_b64_tr_b16 v[218:219], v160 offset:0xa00
	v_mfma_f32_32x32x16_bf16 v[0:15], v[132:135], v[226:229], v[0:15]
	ds_read_b64_tr_b16 v[226:227], v160 offset:0x1200
	ds_read_b64_tr_b16 v[228:229], v160 offset:0x1a00
	v_mfma_f32_32x32x16_bf16 v[0:15], v[136:139], v[236:239], v[0:15]
	ds_read_b64_tr_b16 v[236:237], v160 offset:0x2200
	ds_read_b64_tr_b16 v[238:239], v160 offset:0x2a00
	v_mfma_f32_32x32x16_bf16 v[0:15], v[140:143], v[246:249], v[0:15]
	ds_read_b64_tr_b16 v[246:247], v160 offset:0x3200
	ds_read_b64_tr_b16 v[248:249], v160 offset:0x3a00
	s_waitcnt lgkmcnt(0)
	v_mfma_f32_32x32x16_bf16 v[16:31], v[128:131], v[216:219], v[16:31]
	ds_read_b64_tr_b16 v[216:217], v160 offset:0x400
	ds_read_b64_tr_b16 v[218:219], v160 offset:0xc00
	v_mfma_f32_32x32x16_bf16 v[16:31], v[132:135], v[226:229], v[16:31]
	ds_read_b64_tr_b16 v[226:227], v160 offset:0x1400
	ds_read_b64_tr_b16 v[228:229], v160 offset:0x1c00
	v_mfma_f32_32x32x16_bf16 v[16:31], v[136:139], v[236:239], v[16:31]
	ds_read_b64_tr_b16 v[236:237], v160 offset:0x2400
	ds_read_b64_tr_b16 v[238:239], v160 offset:0x2c00
	v_mfma_f32_32x32x16_bf16 v[16:31], v[140:143], v[246:249], v[16:31]
	ds_read_b64_tr_b16 v[246:247], v160 offset:0x3400
	ds_read_b64_tr_b16 v[248:249], v160 offset:0x3c00
	s_waitcnt lgkmcnt(0)
	v_mfma_f32_32x32x16_bf16 v[32:47], v[128:131], v[216:219], v[32:47]
	ds_read_b64_tr_b16 v[216:217], v160 offset:0x600
	ds_read_b64_tr_b16 v[218:219], v160 offset:0xe00
	v_mfma_f32_32x32x16_bf16 v[32:47], v[132:135], v[226:229], v[32:47]
	ds_read_b64_tr_b16 v[226:227], v160 offset:0x1600
	ds_read_b64_tr_b16 v[228:229], v160 offset:0x1e00
	v_mfma_f32_32x32x16_bf16 v[32:47], v[136:139], v[236:239], v[32:47]
	ds_read_b64_tr_b16 v[236:237], v160 offset:0x2600
	ds_read_b64_tr_b16 v[238:239], v160 offset:0x2e00
	v_mfma_f32_32x32x16_bf16 v[32:47], v[140:143], v[246:249], v[32:47]
	ds_read_b64_tr_b16 v[246:247], v160 offset:0x3600
	ds_read_b64_tr_b16 v[248:249], v160 offset:0x3e00
	s_waitcnt lgkmcnt(0)
	v_mfma_f32_32x32x16_bf16 v[48:63], v[128:131], v[216:219], v[48:63]
	s_and_b64 vcc, exec, s[44:45]
	v_mfma_f32_32x32x16_bf16 v[48:63], v[132:135], v[226:229], v[48:63]
	v_mfma_f32_32x32x16_bf16 v[48:63], v[136:139], v[236:239], v[48:63]
	v_mfma_f32_32x32x16_bf16 v[48:63], v[140:143], v[246:249], v[48:63]
	s_cbranch_vccnz .LBB0_686
	s_waitcnt vmcnt(0)
	s_waitcnt vmcnt(3)
	ds_write_b128 v232, v[146:149] offset:32768
	s_waitcnt vmcnt(2)
	ds_write_b128 v233, v[154:157] offset:32768
	s_waitcnt vmcnt(1)
	ds_write_b128 v234, v[150:153]
	s_waitcnt vmcnt(0)
	ds_write_b128 v235, v[194:197]
	s_branch .LBB0_686
